# c1 chunk loop converts one expert-weight item per task asynchronously (loads fly during the task); ln1 mod-cache fill rewritten; ln1 stores write-through
# speedup vs baseline: 1.0545x; 1.0181x over previous
.LBB0_174:
	s_lshl_b32 s22, s36, 20
	s_lshl_b32 s23, s36, 28
	s_waitcnt vmcnt(3)
	v_mov_b32_e32 v2, v0
	s_mov_b64 s[0:1], s[42:43]
	s_add_u32 s19, s0, 0x10a4c000
	s_addc_u32 s20, s1, 0
	s_add_u32 s2, s0, 0x14a4c000
	s_addc_u32 s3, s1, 0
	s_add_u32 s4, s0, 0x894c000
	s_addc_u32 s5, s1, 0
	v_readfirstlane_b32 s10, v2
	s_add_u32 s21, s0, 0x94c000
	s_addc_u32 s24, s1, 0
	v_lshlrev_b32_e32 v3, 1, v2
	s_ashr_i32 s0, s10, 1
	v_and_b32_e32 v70, 0x70, v3
	s_and_b32 s10, s0, 0xffffffe0
	v_lshlrev_b32_e32 v3, 2, v2
	v_lshlrev_b32_e32 v2, 6, v2
	s_lshr_b32 s0, s0, 1
	s_mov_b32 s18, s85
	s_mov_b32 s26, s95
	v_and_b32_e32 v72, 28, v3
	v_and_b32_e32 v2, 0x80, v2
	s_and_b32 s0, s0, 0x60
	v_and_b32_e32 v3, 4, v3
	s_mov_b32 s25, 7
	s_movk_i32 s56, 0x1817
	s_ashr_i32 s11, s10, 31
	v_or3_b32 v67, v3, v2, s0
	v_mov_b32_e32 v71, v69
	v_or_b32_e32 v73, s0, v2
	s_mov_b32 s27, s26
	s_cmp_ge_u32 s95, 128
	s_cselect_b32 s100, 1, 0
	s_mov_b32 s101, 0
	s_cmp_eq_u32 s100, 0
	s_cbranch_scc0 .LBB0_302
	s_branch .LBB0_177

.LBB0_430:
	s_movk_i32 s34, 0x1000
	s_barrier
	s_cmp_eq_u32 s100, 1
	s_cbranch_scc0 .LBB0_431
	s_mov_b32 s101, 1
	s_lshl_b32 s22, s36, 20
	s_lshl_b32 s23, s36, 28
	s_waitcnt vmcnt(3)
	v_mov_b32_e32 v2, v0
	s_mov_b64 s[0:1], s[42:43]
	s_add_u32 s19, s0, 0x10a4c000
	s_addc_u32 s20, s1, 0
	s_add_u32 s2, s0, 0x14a4c000
	s_addc_u32 s3, s1, 0
	s_add_u32 s4, s0, 0x894c000
	s_addc_u32 s5, s1, 0
	v_readfirstlane_b32 s10, v2
	s_add_u32 s21, s0, 0x94c000
	s_addc_u32 s24, s1, 0
	v_lshlrev_b32_e32 v3, 1, v2
	s_ashr_i32 s0, s10, 1
	v_and_b32_e32 v70, 0x70, v3
	s_and_b32 s10, s0, 0xffffffe0
	v_lshlrev_b32_e32 v3, 2, v2
	v_lshlrev_b32_e32 v2, 6, v2
	s_lshr_b32 s0, s0, 1
	s_mov_b32 s18, s85
	s_mov_b32 s26, s95
	v_and_b32_e32 v72, 28, v3
	v_and_b32_e32 v2, 0x80, v2
	s_and_b32 s0, s0, 0x60
	v_and_b32_e32 v3, 4, v3
	s_mov_b32 s25, 7
	s_movk_i32 s56, 0x1817
	s_ashr_i32 s11, s10, 31
	v_or3_b32 v67, v3, v2, s0
	v_mov_b32_e32 v71, v69
	v_or_b32_e32 v73, s0, v2
	s_mov_b32 s27, s26
	s_branch .LBB0_177

.LBB0_496:
	v_bfe_u32 v48, v20, 2, 6
	v_lshlrev_b32_e32 v19, 3, v14
	v_lshlrev_b32_e32 v14, s3, v48
	v_add_u32_e32 v16, s2, v14
	v_mov_b64_e32 v[14:15], s[16:17]
	v_mad_i64_i32 v[14:15], s[2:3], v16, s33, v[14:15]
	v_and_b32_e32 v68, 48, v22
	v_lshl_add_u64 v[14:15], v[14:15], 0, v[68:69]
	global_load_dwordx4 v[14:17], v[14:15], off offset:1536
	s_add_u32 s0, s18, 0x4e872100
	s_addc_u32 s1, s19, 0
	v_and_b32_e32 v22, 0x70, v22
	s_movk_i32 s10, 0x90
	s_add_i32 s2, 0, 0x1b000
	v_lshl_add_u32 v38, v47, 1, 0
	v_add_u32_e32 v37, s2, v22
	v_mul_u32_u24_e32 v39, 0x90, v22
	v_mad_u32_u24 v49, v22, s10, v38
	v_lshlrev_b32_e32 v22, 5, v20
	v_lshrrev_b32_e32 v23, 2, v20
	v_and_b32_e32 v24, 64, v22
	v_add_u32_e32 v23, v24, v23
	s_movk_i32 s4, 0x44
	v_mul_lo_u32 v23, v23, s4
	v_and_b32_e32 v22, 32, v22
	s_lshl_b32 s8, s20, 3
	v_add3_u32 v50, 0, v23, v22
	s_lshl_b32 s4, s20, 5
	v_mul_u32_u24_e32 v22, 0x48, v21
	s_ashr_i32 s9, s8, 31
	s_add_i32 s31, s4, 0
	s_ashr_i32 s21, s20, 31
	v_add_lshl_u32 v41, s8, v22, 1
	s_lshl_b64 s[8:9], s[8:9], 2
	s_add_u32 s7, s18, s8
	s_addc_u32 s8, s19, s9
	s_add_u32 s34, s7, 0x56c72100
	s_addc_u32 s35, s8, 0
	s_cmp_gt_u32 s30, 1
	s_cselect_b64 s[22:23], -1, 0
	s_and_b64 s[8:9], s[22:23], exec
	v_lshrrev_b32_e32 v22, 4, v21
	s_cselect_b32 s37, 6, 0
	s_bfe_u32 s6, s6, 0x10006
	v_and_b32_e32 v24, 15, v20
	v_lshlrev_b32_e32 v25, 3, v22
	v_lshlrev_b32_e32 v22, 2, v22
	v_lshl_or_b32 v29, s6, 6, v24
	v_lshl_or_b32 v30, s6, 7, v22
	s_lshl_b64 s[6:7], s[20:21], 10
	s_add_u32 s6, s18, s6
	v_lshlrev_b32_e32 v22, 4, v21
	v_mov_b32_e32 v23, v69
	s_addc_u32 s7, s19, s7
	v_lshl_add_u64 v[22:23], s[6:7], 0, v[22:23]
	s_mov_b64 s[6:7], 0x5f17a100
	v_lshl_add_u64 v[26:27], v[22:23], 0, s[6:7]
	s_lshl_b32 s6, s20, 4
	s_and_b32 s7, s6, 0xffffffe0
	v_mul_u32_u24_e32 v40, 0x44, v21
	v_lshl_add_u32 v42, v21, 1, 0
	v_cmp_eq_u32_e64 s[4:5], 0, v21
	v_or_b32_e32 v21, s7, v24
	s_movk_i32 s21, 0x48
	v_or_b32_e32 v28, 32, v25
	v_mul_lo_u32 v21, v21, s21
	v_add_lshl_u32 v44, v21, v25, 1
	v_add_lshl_u32 v45, v21, v28, 1
	v_add_u32_e32 v21, s7, v30
	v_mul_lo_u32 v64, v21, s10
	v_mad_u32_u24 v21, v29, s21, v240
	v_add_lshl_u32 v65, v21, v25, 1
	v_add_lshl_u32 v67, v21, v28, 1
	v_mad_u32_u24 v21, v29, s21, v241
	v_add_lshl_u32 v70, v21, v25, 1
	v_add_lshl_u32 v71, v21, v28, 1
	v_mad_u32_u24 v21, v29, s21, v242
	s_or_b32 s6, s6, 16
	v_add_lshl_u32 v72, v21, v25, 1
	v_add_lshl_u32 v73, v21, v28, 1
	v_or_b32_e32 v21, s6, v24
	v_mul_lo_u32 v21, v21, s21
	v_ashrrev_i32_e32 v51, 10, v20
	v_bfe_u32 v33, v20, 3, 7
	v_add_lshl_u32 v74, v21, v25, 1
	v_add_lshl_u32 v75, v21, v28, 1
	v_add_u32_e32 v21, s6, v30
	v_mul_u32_u24_e32 v22, 0x48, v29
	v_mul_lo_u32 v76, v21, s10
	v_lshl_or_b32 v21, v51, 7, v33
	v_and_b32_e32 v32, 56, v46
	v_add_lshl_u32 v62, v22, v25, 1
	v_add_lshl_u32 v63, v22, v28, 1
	v_mul_lo_u32 v21, v21, s21
	v_lshlrev_b32_e32 v22, 7, v33
	v_mov_b32_e32 v23, v69
	v_lshl_add_u32 v43, v24, 1, s92
	v_add_lshl_u32 v77, v21, v32, 1
	v_lshl_add_u64 v[22:23], s[0:1], 0, v[22:23]
	v_lshlrev_b32_e32 v24, 1, v32
	v_mov_b32_e32 v25, v69
	v_add_u32_e32 v21, 0x200, v20
	v_lshl_add_u64 v[28:29], v[22:23], 0, v[24:25]
	v_ashrrev_i32_e32 v52, 10, v21
	v_bfe_u32 v22, v21, 3, 7
	v_cmp_gt_u32_e64 s[8:9], s90, v21
	v_lshl_or_b32 v21, v52, 7, v22
	v_mul_lo_u32 v21, v21, s21
	v_add_lshl_u32 v78, v21, v32, 1
	v_add_u32_e32 v21, 0x400, v20
	v_ashrrev_i32_e32 v53, 10, v21
	v_mul_lo_u32 v36, v47, s10
	s_movk_i32 s2, 0x100
	v_lshlrev_b32_e32 v22, 7, v22
	v_mov_b32_e32 v23, v69
	s_movk_i32 s10, 0xfbff
	v_lshl_or_b32 v21, v53, 7, v33
	v_cmp_gt_i32_e64 s[2:3], s2, v20
	v_cmp_gt_u32_e64 s[6:7], s90, v20
	v_lshl_add_u64 v[22:23], s[0:1], 0, v[22:23]
	v_cmp_lt_u32_e64 s[10:11], s10, v20
	v_mul_lo_u32 v21, v21, s21
	v_add_u32_e32 v20, 0x600, v20
	v_lshl_add_u64 v[30:31], v[22:23], 0, v[24:25]
	v_add_lshl_u32 v22, v21, v32, 1
	v_ashrrev_i32_e32 v54, 10, v20
	v_bfe_u32 v21, v20, 3, 7
	v_cmp_gt_u32_e64 s[12:13], s90, v20
	v_lshl_or_b32 v20, v54, 7, v21
	v_mul_lo_u32 v20, v20, s21
	v_add_lshl_u32 v23, v20, v32, 1
	v_lshlrev_b32_e32 v20, 7, v21
	v_mov_b32_e32 v21, v69
	v_lshl_add_u64 v[20:21], s[0:1], 0, v[20:21]
	s_lshl_b32 s0, s25, 6
	s_mul_i32 s15, s20, 0x480
	v_lshl_add_u64 v[32:33], v[20:21], 0, v[24:25]
	s_add_i32 s40, s0, 0x1300
	s_lshl_b32 s0, s25, 12
	v_add_u32_e32 v20, 0, v41
	v_lshl_add_u64 v[34:35], s[16:17], 0, v[68:69]
	s_mul_i32 s21, s30, 0x108
	s_lshl_b32 s38, s25, 1
	s_sub_i32 s39, 0, s25
	s_add_i32 s41, s0, 0x40000
	v_add_u32_e32 v55, v37, v36
	v_add_u32_e32 v56, v38, v39
	v_add_u32_e32 v57, 0, v40
	v_add_u32_e32 v58, 0x1b000, v20
	v_add_u32_e32 v59, s15, v42
	v_lshlrev_b32_e32 v68, 1, v19
	s_lshl_b32 s24, s14, 1
	v_lshlrev_b32_e32 v36, 1, v18
	v_add_u32_e32 v60, 0, v44
	v_add_u32_e32 v61, 0, v45
	v_add_u32_e32 v62, 0, v62
	v_add_u32_e32 v63, 0, v63
	v_add_u32_e32 v64, v43, v64
	v_add_u32_e32 v65, 0, v65
	v_add_u32_e32 v67, 0, v67
	v_add_u32_e32 v70, 0, v70
	v_add_u32_e32 v71, 0, v71
	v_add_u32_e32 v72, 0, v72
	v_add_u32_e32 v73, 0, v73
	v_add_u32_e32 v74, 0, v74
	v_add_u32_e32 v75, 0, v75
	v_add_u32_e32 v76, v43, v76
	v_add_u32_e32 v77, s92, v77
	v_add_u32_e32 v78, s92, v78
	v_add_u32_e32 v79, s92, v22
	v_add_u32_e32 v80, s92, v23
	s_add_i32 vcc_lo, s95, 0x700
	v_writelane_b32 v246, vcc_lo, 48
	s_mov_b32 vcc_lo, 8
	v_writelane_b32 v246, vcc_lo, 50
	s_mov_b32 vcc_lo, 0
	v_writelane_b32 v246, vcc_lo, 49
	s_branch .LBB0_499

.LBB0_498:
	s_waitcnt lgkmcnt(0)
	s_barrier
	ds_read_b128 v[18:21], v60 offset:54272
	ds_read_b128 v[22:25], v61 offset:54272
	ds_read_b128 v[38:41], v62 offset:17408
	ds_read_b128 v[42:45], v63 offset:17408
	s_mul_i32 s0, s45, 0x84
	s_waitcnt lgkmcnt(1)
	v_mfma_f32_16x16x32_bf16 v[38:41], v[18:21], v[38:41], 0
	s_lshl_b32 s1, s30, 1
	s_lshl_b32 s25, s45, 3
	s_or_b32 s1, s25, s1
	s_waitcnt lgkmcnt(0)
	v_mfma_f32_16x16x32_bf16 v[38:41], v[22:25], v[42:45], v[38:41]
	s_cmp_gt_i32 s44, 3
	s_cselect_b32 s25, 0x87, 3
	s_add_i32 s25, s25, s0
	s_addk_i32 s38, 0x80
	s_addk_i32 s40, 0x1000
	s_nop 2
	v_cvt_pk_bf16_f32 v37, v38, s0
	ds_write_b16 v64, v37
	v_cvt_pk_bf16_f32 v37, v39, s0
	ds_write_b16 v64, v37 offset:144
	v_cvt_pk_bf16_f32 v37, v40, s0
	ds_write_b16 v64, v37 offset:288
	v_cvt_pk_bf16_f32 v37, v41, s0
	ds_write_b16 v64, v37 offset:432
	ds_read_b128 v[38:41], v65 offset:17408
	ds_read_b128 v[42:45], v67 offset:17408
	s_waitcnt lgkmcnt(1)
	v_mfma_f32_16x16x32_bf16 v[38:41], v[18:21], v[38:41], 0
	s_add_i32 s41, s41, 0x40000
	s_and_b64 vcc, exec, s[14:15]
	s_waitcnt lgkmcnt(0)
	v_mfma_f32_16x16x32_bf16 v[38:41], v[22:25], v[42:45], v[38:41]
	s_nop 7
	v_cvt_pk_bf16_f32 v37, v38, s0
	ds_write_b16 v64, v37 offset:32
	v_cvt_pk_bf16_f32 v37, v39, s0
	ds_write_b16 v64, v37 offset:176
	v_cvt_pk_bf16_f32 v37, v40, s0
	ds_write_b16 v64, v37 offset:320
	v_cvt_pk_bf16_f32 v37, v41, s0
	ds_write_b16 v64, v37 offset:464
	ds_read_b128 v[38:41], v70 offset:17408
	ds_read_b128 v[42:45], v71 offset:17408
	s_waitcnt lgkmcnt(1)
	v_mfma_f32_16x16x32_bf16 v[38:41], v[18:21], v[38:41], 0
	s_waitcnt lgkmcnt(0)
	v_mfma_f32_16x16x32_bf16 v[38:41], v[22:25], v[42:45], v[38:41]
	s_nop 7
	v_cvt_pk_bf16_f32 v37, v38, s0
	ds_write_b16 v64, v37 offset:64
	v_cvt_pk_bf16_f32 v37, v39, s0
	ds_write_b16 v64, v37 offset:208
	v_cvt_pk_bf16_f32 v37, v40, s0
	ds_write_b16 v64, v37 offset:352
	v_cvt_pk_bf16_f32 v37, v41, s0
	ds_write_b16 v64, v37 offset:496
	ds_read_b128 v[38:41], v72 offset:17408
	ds_read_b128 v[42:45], v73 offset:17408
	s_waitcnt lgkmcnt(1)
	v_mfma_f32_16x16x32_bf16 v[18:21], v[18:21], v[38:41], 0
	s_waitcnt lgkmcnt(0)
	v_mfma_f32_16x16x32_bf16 v[18:21], v[22:25], v[42:45], v[18:21]
	s_nop 7
	v_cvt_pk_bf16_f32 v18, v18, s0
	ds_write_b16 v64, v18 offset:96
	v_cvt_pk_bf16_f32 v18, v19, s0
	ds_write_b16 v64, v18 offset:240
	v_cvt_pk_bf16_f32 v18, v20, s0
	ds_write_b16 v64, v18 offset:384
	v_cvt_pk_bf16_f32 v18, v21, s0
	ds_write_b16 v64, v18 offset:528
	ds_read_b128 v[18:21], v74 offset:54272
	ds_read_b128 v[22:25], v75 offset:54272
	ds_read_b128 v[38:41], v62 offset:17408
	ds_read_b128 v[42:45], v63 offset:17408
	s_waitcnt lgkmcnt(1)
	v_mfma_f32_16x16x32_bf16 v[38:41], v[18:21], v[38:41], 0
	s_waitcnt lgkmcnt(0)
	v_mfma_f32_16x16x32_bf16 v[38:41], v[22:25], v[42:45], v[38:41]
	s_nop 7
	v_cvt_pk_bf16_f32 v37, v38, s0
	ds_write_b16 v76, v37
	v_cvt_pk_bf16_f32 v37, v39, s0
	ds_write_b16 v76, v37 offset:144
	v_cvt_pk_bf16_f32 v37, v40, s0
	ds_write_b16 v76, v37 offset:288
	v_cvt_pk_bf16_f32 v37, v41, s0
	ds_write_b16 v76, v37 offset:432
	ds_read_b128 v[38:41], v65 offset:17408
	ds_read_b128 v[42:45], v67 offset:17408
	s_waitcnt lgkmcnt(1)
	v_mfma_f32_16x16x32_bf16 v[38:41], v[18:21], v[38:41], 0
	s_waitcnt lgkmcnt(0)
	v_mfma_f32_16x16x32_bf16 v[38:41], v[22:25], v[42:45], v[38:41]
	s_nop 7
	v_cvt_pk_bf16_f32 v37, v38, s0
	ds_write_b16 v76, v37 offset:32
	v_cvt_pk_bf16_f32 v37, v39, s0
	ds_write_b16 v76, v37 offset:176
	v_cvt_pk_bf16_f32 v37, v40, s0
	ds_write_b16 v76, v37 offset:320
	v_cvt_pk_bf16_f32 v37, v41, s0
	ds_write_b16 v76, v37 offset:464
	ds_read_b128 v[38:41], v70 offset:17408
	ds_read_b128 v[42:45], v71 offset:17408
	s_waitcnt lgkmcnt(1)
	v_mfma_f32_16x16x32_bf16 v[38:41], v[18:21], v[38:41], 0
	s_waitcnt lgkmcnt(0)
	v_mfma_f32_16x16x32_bf16 v[38:41], v[22:25], v[42:45], v[38:41]
	s_nop 7
	v_cvt_pk_bf16_f32 v37, v38, s0
	ds_write_b16 v76, v37 offset:64
	v_cvt_pk_bf16_f32 v37, v39, s0
	ds_write_b16 v76, v37 offset:208
	v_cvt_pk_bf16_f32 v37, v40, s0
	ds_write_b16 v76, v37 offset:352
	v_cvt_pk_bf16_f32 v37, v41, s0
	ds_write_b16 v76, v37 offset:496
	ds_read_b128 v[38:41], v72 offset:17408
	ds_read_b128 v[42:45], v73 offset:17408
	s_waitcnt lgkmcnt(1)
	v_mfma_f32_16x16x32_bf16 v[18:21], v[18:21], v[38:41], 0
	s_waitcnt lgkmcnt(0)
	v_mfma_f32_16x16x32_bf16 v[18:21], v[22:25], v[42:45], v[18:21]
	v_mov_b32_e32 v25, s44
	s_nop 6
	v_cvt_pk_bf16_f32 v18, v18, s0
	ds_write_b16 v76, v18 offset:96
	v_cvt_pk_bf16_f32 v18, v19, s0
	ds_write_b16 v76, v18 offset:240
	v_cvt_pk_bf16_f32 v18, v20, s0
	ds_write_b16 v76, v18 offset:384
	v_cvt_pk_bf16_f32 v18, v21, s0
	s_add_i32 s0, s39, s25
	v_mov_b32_e32 v24, s0
	ds_write_b16 v76, v18 offset:528
	v_cndmask_b32_e64 v18, v24, v25, s[6:7]
	s_waitcnt lgkmcnt(0)
	s_barrier
	v_add_u32_e32 v20, s1, v51
	v_ashrrev_i32_e32 v19, 31, v18
	s_movk_i32 s0, 0x84
	v_mad_i64_i32 v[22:23], s[26:27], v20, s0, v[18:19]
	ds_read_b128 v[18:21], v77
	v_lshlrev_b64 v[22:23], 14, v[22:23]
	v_lshl_add_u64 v[22:23], v[28:29], 0, v[22:23]
	s_sub_i32 s39, s39, 64
	s_mov_b32 s25, s48
	s_waitcnt lgkmcnt(0)
	global_store_dwordx4 v[22:23], v[18:21], off
	s_nop 1
	v_cndmask_b32_e64 v18, v24, v25, s[8:9]
	v_add_u32_e32 v20, s1, v52
	v_ashrrev_i32_e32 v19, 31, v18
	v_mad_i64_i32 v[22:23], s[26:27], v20, s0, v[18:19]
	ds_read_b128 v[18:21], v78
	v_lshlrev_b64 v[22:23], 14, v[22:23]
	v_lshl_add_u64 v[22:23], v[30:31], 0, v[22:23]
	s_waitcnt lgkmcnt(0)
	global_store_dwordx4 v[22:23], v[18:21], off
	s_nop 1
	v_cndmask_b32_e64 v18, v24, v25, s[10:11]
	v_add_u32_e32 v20, s1, v53
	v_ashrrev_i32_e32 v19, 31, v18
	v_mad_i64_i32 v[22:23], s[26:27], v20, s0, v[18:19]
	ds_read_b128 v[18:21], v79
	v_lshlrev_b64 v[22:23], 14, v[22:23]
	v_lshl_add_u64 v[22:23], v[28:29], 0, v[22:23]
	s_waitcnt lgkmcnt(0)
	global_store_dwordx4 v[22:23], v[18:21], off
	s_nop 1
	v_cndmask_b32_e64 v18, v24, v25, s[12:13]
	v_add_u32_e32 v20, s1, v54
	v_ashrrev_i32_e32 v19, 31, v18
	v_mad_i64_i32 v[22:23], s[0:1], v20, s0, v[18:19]
	ds_read_b128 v[18:21], v80
	v_lshlrev_b64 v[22:23], 14, v[22:23]
	v_lshl_add_u64 v[22:23], v[32:33], 0, v[22:23]
	s_waitcnt lgkmcnt(0)
	global_store_dwordx4 v[22:23], v[18:21], off
	v_writelane_b32 v246, s12, 0
	v_writelane_b32 v246, s13, 1
	v_writelane_b32 v246, s14, 2
	v_writelane_b32 v246, s16, 3
	v_writelane_b32 v246, s28, 4
	v_writelane_b32 v246, s29, 5
	v_writelane_b32 v246, s30, 6
	v_writelane_b32 v246, vcc_lo, 33
	v_writelane_b32 v246, vcc_hi, 34
	s_nop 1
	v_readlane_b32 s26, v246, 49
	s_nop 1
	s_cmp_eq_u32 s26, 0
	s_cbranch_scc1 .Lc1_cskip
	v_readlane_b32 s12, v246, 40
	v_readlane_b32 s13, v246, 41
	v_readlane_b32 s16, v246, 42
	v_readlane_b32 s28, v246, 43
	v_readlane_b32 s29, v246, 44
	v_readlane_b32 s30, v246, 45
	s_mov_b32 s26, 0
	v_writelane_b32 v246, s26, 49
	s_waitcnt vmcnt(0)
	s_cmp_lt_i32 s30, 1
	s_cbranch_scc1 .Lc1c_194
	s_cmp_gt_i32 s30, 1
	s_cbranch_scc0 .Lc1c_195
	s_cmp_eq_u32 s30, 2
	s_mov_b64 s[0:1], -1
	s_cbranch_scc0 .Lc1c_193
	s_lshl_b32 s0, s16, 1
	v_and_b32_e32 v174, 0x7c, v181
	s_and_b32 s0, s0, 0xffffff00
	v_or_b32_e32 v174, s0, v174
	v_or_b32_e32 v174, 0x80, v174
	s_mov_b64 s[0:1], 0

.Lc1c_195:
	s_mov_b64 s[0:1], 0
	s_cbranch_execz .Lc1c_197
	s_lshl_b32 s14, s16, 1
	v_and_b32_e32 v174, 0x7c, v181
	s_and_b32 s14, s14, 0xffffff00
	v_or_b32_e32 v174, s14, v174

.Lc1c_198:
	s_cmp_lg_u32 s30, 0
	s_cselect_b64 s[0:1], -1, 0
	v_mov_b32_e32 v174, v181
.Lc1c_199:
	s_andn2_b64 vcc, exec, s[0:1]
	v_lshrrev_b32_e32 v180, 1, v181
	s_cbranch_vccnz .Lc1c_201
	s_and_b32 s0, s16, 0xffffff00
	v_and_b32_e32 v174, 24, v180
	v_or3_b32 v174, s0, v174, v173
.Lc1c_201:
	v_mul_f32_e32 v112, 0x42000000, v112
	v_mul_f32_e32 v116, 0x42000000, v116
	v_mov_b32_e32 v182, v175
	v_cvt_pk_fp8_f32 v182, v112, v116
	v_mul_f32_e32 v112, 0x42000000, v140
	v_mul_f32_e32 v116, 0x42000000, v144
	v_mul_f32_e32 v140, 0x42000000, v164
	v_mul_f32_e32 v144, 0x42000000, v168
	v_mov_b32_e32 v183, v175
	v_cvt_pk_fp8_f32 v183, v140, v144
	v_cvt_pk_fp8_f32 v182, v112, v116 op_sel:[0,0,1]
	v_mul_f32_e32 v112, 0x42000000, v120
	v_mul_f32_e32 v116, 0x42000000, v148
	v_cvt_pk_fp8_f32 v183, v112, v116 op_sel:[0,0,1]
	v_mul_f32_e32 v112, 0x42000000, v124
	v_mul_f32_e32 v116, 0x42000000, v152
	v_mov_b32_e32 v184, v175
	v_cvt_pk_fp8_f32 v184, v112, v116
	v_mul_f32_e32 v120, 0x42000000, v132
	v_mul_f32_e32 v124, 0x42000000, v160
	v_mov_b32_e32 v185, v175
	v_cvt_pk_fp8_f32 v185, v120, v124
	v_mul_f32_e32 v112, 0x42000000, v128
	v_mul_f32_e32 v116, 0x42000000, v156
	v_cvt_pk_fp8_f32 v184, v112, v116 op_sel:[0,0,1]
	v_mul_f32_e32 v108, 0x42000000, v108
	v_mul_f32_e32 v112, 0x42000000, v136
	v_cvt_pk_fp8_f32 v185, v108, v112 op_sel:[0,0,1]
	v_lshrrev_b32_e32 v108, 8, v174
	v_mov_b32_e32 v112, s28
	v_mad_i32_i24 v186, v108, s29, v112
	v_ashrrev_i32_e32 v187, 31, v186
	v_lshlrev_b64 v[186:187], 15, v[186:187]
	v_lshlrev_b32_e32 v108, 7, v174
	v_and_b32_e32 v174, 0x7f80, v108
	v_lshl_add_u64 v[186:187], s[12:13], 0, v[186:187]
	v_lshl_add_u64 v[186:187], v[186:187], 0, v[174:175]
	v_lshl_add_u64 v[186:187], v[186:187], 0, v[176:177]
	s_cmp_lt_i32 s30, 1
	v_or_b32_e32 v112, 1, v181
	global_store_dwordx4 v[186:187], v[182:185], off
	s_cbranch_scc1 .Lc1c_206
	s_cmp_gt_i32 s30, 1
	s_cbranch_scc0 .Lc1c_207
	s_cmp_eq_u32 s30, 2
	s_mov_b64 s[0:1], -1
	s_cbranch_scc0 .Lc1c_205
	s_lshl_b32 s0, s16, 1
	v_and_b32_e32 v108, 0x7d, v112
	s_and_b32 s0, s0, 0xffffff00
	v_or_b32_e32 v108, s0, v108
	v_or_b32_e32 v108, 0x80, v108
	s_mov_b64 s[0:1], 0

.Lc1c_207:
	s_mov_b64 s[0:1], 0
	s_cbranch_execz .Lc1c_209
	s_lshl_b32 s14, s16, 1
	v_and_b32_e32 v108, 0x7d, v112
	s_and_b32 s14, s14, 0xffffff00
	v_or_b32_e32 v108, s14, v108

.Lc1c_210:
	s_cmp_lg_u32 s30, 0
	s_cselect_b64 s[0:1], -1, 0
	v_mov_b32_e32 v108, v112
.Lc1c_211:
	s_andn2_b64 vcc, exec, s[0:1]
	s_cbranch_vccnz .Lc1c_213
	s_and_b32 s0, s16, 0xffffff00
	v_and_b32_e32 v108, 5, v112
	v_and_or_b32 v112, v180, 24, s0
	v_or3_b32 v108, v112, v108, v179
.Lc1c_213:
	v_mul_f32_e32 v112, 0x42000000, v113
	v_mul_f32_e32 v113, 0x42000000, v117
	v_mov_b32_e32 v182, v175
	v_cvt_pk_fp8_f32 v182, v112, v113
	v_mul_f32_e32 v116, 0x42000000, v165
	v_mul_f32_e32 v117, 0x42000000, v169
	v_mov_b32_e32 v183, v175
	v_cvt_pk_fp8_f32 v183, v116, v117
	v_mul_f32_e32 v112, 0x42000000, v141
	v_mul_f32_e32 v113, 0x42000000, v145
	v_cvt_pk_fp8_f32 v182, v112, v113 op_sel:[0,0,1]
	v_mul_f32_e32 v112, 0x42000000, v121
	v_mul_f32_e32 v113, 0x42000000, v149
	v_cvt_pk_fp8_f32 v183, v112, v113 op_sel:[0,0,1]
	v_mul_f32_e32 v112, 0x42000000, v125
	v_mul_f32_e32 v113, 0x42000000, v153
	v_mov_b32_e32 v184, v175
	v_cvt_pk_fp8_f32 v184, v112, v113
	v_mul_f32_e32 v116, 0x42000000, v133
	v_mul_f32_e32 v117, 0x42000000, v161
	v_mov_b32_e32 v185, v175
	v_cvt_pk_fp8_f32 v185, v116, v117
	v_mul_f32_e32 v112, 0x42000000, v129
	v_mul_f32_e32 v113, 0x42000000, v157
	v_cvt_pk_fp8_f32 v184, v112, v113 op_sel:[0,0,1]
	v_mul_f32_e32 v109, 0x42000000, v109
	v_mul_f32_e32 v112, 0x42000000, v137
	v_cvt_pk_fp8_f32 v185, v109, v112 op_sel:[0,0,1]
	v_lshrrev_b32_e32 v109, 8, v108
	v_mov_b32_e32 v112, s28
	v_mad_i32_i24 v112, v109, s29, v112
	v_ashrrev_i32_e32 v113, 31, v112
	v_lshlrev_b64 v[112:113], 15, v[112:113]
	v_lshlrev_b32_e32 v108, 7, v108
	v_and_b32_e32 v174, 0x7f80, v108
	v_lshl_add_u64 v[108:109], s[12:13], 0, v[112:113]
	v_lshl_add_u64 v[108:109], v[108:109], 0, v[174:175]
	v_lshl_add_u64 v[108:109], v[108:109], 0, v[176:177]
	global_store_dwordx4 v[108:109], v[182:185], off
	s_cmp_lt_i32 s30, 1
	v_or_b32_e32 v109, 2, v181
	s_cbranch_scc1 .Lc1c_218
	s_cmp_gt_i32 s30, 1
	s_cbranch_scc0 .Lc1c_219
	s_cmp_eq_u32 s30, 2
	s_mov_b64 s[0:1], -1
	s_cbranch_scc0 .Lc1c_217
	s_lshl_b32 s0, s16, 1
	v_and_b32_e32 v108, 0x7e, v109
	s_and_b32 s0, s0, 0xffffff00
	v_or_b32_e32 v108, s0, v108
	v_or_b32_e32 v108, 0x80, v108
	s_mov_b64 s[0:1], 0

.Lc1c_219:
	s_mov_b64 s[0:1], 0
	s_cbranch_execz .Lc1c_221
	s_lshl_b32 s14, s16, 1
	v_and_b32_e32 v108, 0x7e, v109
	s_and_b32 s14, s14, 0xffffff00
	v_or_b32_e32 v108, s14, v108

.Lc1c_222:
	s_cmp_lg_u32 s30, 0
	s_cselect_b64 s[0:1], -1, 0
	v_mov_b32_e32 v108, v109
.Lc1c_223:
	s_andn2_b64 vcc, exec, s[0:1]
	s_cbranch_vccnz .Lc1c_225
	s_and_b32 s0, s16, 0xffffff00
	v_and_b32_e32 v108, 6, v109
	v_and_or_b32 v109, v180, 24, s0
	v_or3_b32 v108, v109, v108, v179
.Lc1c_225:
	v_mul_f32_e32 v109, 0x42000000, v114
	v_mul_f32_e32 v112, 0x42000000, v118
	v_mov_b32_e32 v182, v175
	v_cvt_pk_fp8_f32 v182, v109, v112
	v_mul_f32_e32 v113, 0x42000000, v166
	v_mul_f32_e32 v114, 0x42000000, v170
	v_mov_b32_e32 v183, v175
	v_cvt_pk_fp8_f32 v183, v113, v114
	v_mul_f32_e32 v109, 0x42000000, v142
	v_mul_f32_e32 v112, 0x42000000, v146
	v_cvt_pk_fp8_f32 v182, v109, v112 op_sel:[0,0,1]
	v_mul_f32_e32 v109, 0x42000000, v122
	v_mul_f32_e32 v112, 0x42000000, v150
	v_cvt_pk_fp8_f32 v183, v109, v112 op_sel:[0,0,1]
	v_mul_f32_e32 v109, 0x42000000, v126
	v_mul_f32_e32 v112, 0x42000000, v154
	v_mov_b32_e32 v184, v175
	v_cvt_pk_fp8_f32 v184, v109, v112
	v_mul_f32_e32 v113, 0x42000000, v134
	v_mul_f32_e32 v114, 0x42000000, v162
	v_mov_b32_e32 v185, v175
	v_cvt_pk_fp8_f32 v185, v113, v114
	v_mul_f32_e32 v109, 0x42000000, v130
	v_mul_f32_e32 v112, 0x42000000, v158
	v_cvt_pk_fp8_f32 v184, v109, v112 op_sel:[0,0,1]
	v_mul_f32_e32 v109, 0x42000000, v110
	v_mul_f32_e32 v110, 0x42000000, v138
	v_cvt_pk_fp8_f32 v185, v109, v110 op_sel:[0,0,1]
	v_lshrrev_b32_e32 v109, 8, v108
	v_mov_b32_e32 v110, s28
	v_mad_i32_i24 v112, v109, s29, v110
	v_ashrrev_i32_e32 v113, 31, v112
	v_lshlrev_b64 v[112:113], 15, v[112:113]
	v_lshlrev_b32_e32 v108, 7, v108
	v_and_b32_e32 v174, 0x7f80, v108
	v_lshl_add_u64 v[108:109], s[12:13], 0, v[112:113]
	v_lshl_add_u64 v[108:109], v[108:109], 0, v[174:175]
	v_lshl_add_u64 v[108:109], v[108:109], 0, v[176:177]
	global_store_dwordx4 v[108:109], v[182:185], off
	s_cmp_lt_i32 s30, 1
	v_or_b32_e32 v109, 3, v181
	s_cbranch_scc1 .Lc1c_230
	s_cmp_gt_i32 s30, 1
	s_cbranch_scc0 .Lc1c_231
	s_cmp_eq_u32 s30, 2
	s_mov_b64 s[0:1], -1
	s_cbranch_scc0 .Lc1c_229
	s_lshl_b32 s0, s16, 1
	v_and_b32_e32 v108, 0x7f, v109
	s_and_b32 s0, s0, 0xffffff00
	v_or_b32_e32 v108, s0, v108
	v_or_b32_e32 v108, 0x80, v108
	s_mov_b64 s[0:1], 0

.Lc1c_231:
	s_mov_b64 s[0:1], 0
	s_cbranch_execz .Lc1c_233
	s_lshl_b32 s14, s16, 1
	v_and_b32_e32 v108, 0x7f, v109
	s_and_b32 s14, s14, 0xffffff00
	v_or_b32_e32 v108, s14, v108

.Lc1c_235:
	s_andn2_b64 vcc, exec, s[0:1]
	s_cbranch_vccnz .Lc1c_175
	s_and_b32 s0, s16, 0xffffff00
	v_and_b32_e32 v108, 7, v109
	v_and_or_b32 v109, v180, 24, s0
	v_or3_b32 v108, v109, v108, v179
	s_branch .Lc1c_175
.Lc1c_175:
	v_mul_f32_e32 v109, 0x42000000, v115
	v_mul_f32_e32 v110, 0x42000000, v119
	v_mov_b32_e32 v112, v175
	v_cvt_pk_fp8_f32 v112, v109, v110
	v_mul_f32_e32 v114, 0x42000000, v167
	v_mul_f32_e32 v115, 0x42000000, v171
	v_mov_b32_e32 v113, v175
	v_cvt_pk_fp8_f32 v113, v114, v115
	v_mul_f32_e32 v109, 0x42000000, v143
	v_mul_f32_e32 v110, 0x42000000, v147
	v_cvt_pk_fp8_f32 v112, v109, v110 op_sel:[0,0,1]
	v_mul_f32_e32 v109, 0x42000000, v123
	v_mul_f32_e32 v110, 0x42000000, v151
	v_cvt_pk_fp8_f32 v113, v109, v110 op_sel:[0,0,1]
	v_mul_f32_e32 v109, 0x42000000, v127
	v_mul_f32_e32 v110, 0x42000000, v155
	v_mov_b32_e32 v114, v175
	v_cvt_pk_fp8_f32 v114, v109, v110
	v_mul_f32_e32 v116, 0x42000000, v135
	v_mul_f32_e32 v117, 0x42000000, v163
	v_mov_b32_e32 v115, v175
	v_cvt_pk_fp8_f32 v115, v116, v117
	v_mul_f32_e32 v109, 0x42000000, v131
	v_mul_f32_e32 v110, 0x42000000, v159
	v_cvt_pk_fp8_f32 v114, v109, v110 op_sel:[0,0,1]
	v_mul_f32_e32 v109, 0x42000000, v111
	v_mul_f32_e32 v110, 0x42000000, v139
	v_cvt_pk_fp8_f32 v115, v109, v110 op_sel:[0,0,1]
	v_lshrrev_b32_e32 v109, 8, v108
	v_mov_b32_e32 v110, s28
	v_mad_i32_i24 v110, v109, s29, v110
	v_ashrrev_i32_e32 v111, 31, v110
	v_lshlrev_b64 v[110:111], 15, v[110:111]
	v_lshlrev_b32_e32 v108, 7, v108
	v_and_b32_e32 v174, 0x7f80, v108
	v_lshl_add_u64 v[108:109], s[12:13], 0, v[110:111]
	v_lshl_add_u64 v[108:109], v[108:109], 0, v[174:175]
	v_lshl_add_u64 v[108:109], v[108:109], 0, v[176:177]
	global_store_dwordx4 v[108:109], v[112:115], off
.Lc1_cskip:
	v_readlane_b32 s0, v246, 33
	v_readlane_b32 s1, v246, 34
	s_nop 1
	s_mov_b64 vcc, s[0:1]
	v_readlane_b32 s12, v246, 0
	v_readlane_b32 s13, v246, 1
	v_readlane_b32 s14, v246, 2
	v_readlane_b32 s16, v246, 3
	v_readlane_b32 s28, v246, 4
	v_readlane_b32 s29, v246, 5
	v_readlane_b32 s30, v246, 6
	s_nop 4
	s_cbranch_vccnz .LBB0_512

.LBB0_501:
	s_or_b64 exec, exec, s[0:1]
	s_waitcnt lgkmcnt(0)
	s_barrier
	v_writelane_b32 v246, s2, 0
	v_writelane_b32 v246, s3, 1
	v_writelane_b32 v246, s4, 2
	v_writelane_b32 v246, s5, 3
	v_writelane_b32 v246, s10, 4
	v_writelane_b32 v246, s11, 5
	v_writelane_b32 v246, s12, 6
	v_writelane_b32 v246, s13, 7
	v_writelane_b32 v246, s16, 8
	v_writelane_b32 v246, s17, 9
	v_writelane_b32 v246, s19, 10
	v_writelane_b32 v246, s20, 11
	v_writelane_b32 v246, s21, 12
	v_writelane_b32 v246, s22, 13
	v_writelane_b32 v246, s23, 14
	v_writelane_b32 v246, s24, 15
	v_writelane_b32 v246, s28, 16
	v_writelane_b32 v246, s29, 17
	v_writelane_b32 v246, s30, 18
	v_writelane_b32 v246, s31, 19
	v_writelane_b32 v246, s66, 20
	s_nop 1
	v_readlane_b32 s27, v246, 48
	v_readlane_b32 s26, v246, 50
	s_nop 1
	s_cmp_eq_u32 s26, 0
	s_cbranch_scc1 .Lc1_iskip
	s_add_i32 s26, s26, -1
	v_writelane_b32 v246, s26, 50
	s_add_i32 s26, s27, 0x100
	v_writelane_b32 v246, s26, 48
	v_mov_b32_e32 v175, 0
	v_readlane_b32 s22, v247, 34
	v_mov_b32_e32 v108, v0
	s_mov_b64 s[0:1], s[42:43]
	s_add_u32 s19, s0, 0x10a4c000
	s_addc_u32 s20, s1, 0
	s_add_u32 s2, s0, 0x14a4c000
	s_addc_u32 s3, s1, 0
	s_add_u32 s4, s0, 0x894c000
	s_addc_u32 s5, s1, 0
	v_readfirstlane_b32 s10, v108
	s_add_u32 s21, s0, 0x94c000
	s_addc_u32 s24, s1, 0
	v_lshlrev_b32_e32 v109, 1, v108
	s_ashr_i32 s0, s10, 1
	v_and_b32_e32 v176, 0x70, v109
	s_and_b32 s10, s0, 0xffffffe0
	v_lshlrev_b32_e32 v109, 2, v108
	v_lshlrev_b32_e32 v108, 6, v108
	s_lshr_b32 s0, s0, 1
	s_and_b32 s23, s22, 0x10000000
	s_and_b32 s22, s22, 0x100000
	v_and_b32_e32 v178, 28, v109
	v_and_b32_e32 v108, 0x80, v108
	s_and_b32 s0, s0, 0x60
	v_and_b32_e32 v109, 4, v109
	s_ashr_i32 s11, s10, 31
	v_or3_b32 v173, v109, v108, s0
	v_mov_b32_e32 v177, v175
	v_or_b32_e32 v179, s0, v108
	s_cmpk_gt_i32 s27, 0xfff
	s_mov_b64 s[16:17], -1
	s_cbranch_scc0 .Lc1i_187
	s_cmpk_gt_u32 s27, 0x17ff
	s_cbranch_scc0 .Lc1i_184
	s_add_i32 s14, s27, 0xffffe800
	s_and_b32 s16, s27, 7
	s_cmp_gt_u32 s14, 15
	s_mov_b64 s[12:13], -1
	s_cbranch_scc0 .Lc1i_182
	v_mov_b32_e32 v108, 0x23f98
	s_mov_b64 s[12:13], 0
	v_add_u32_e32 v108, 0, v108
	ds_read_b64 v[108:109], v108
	s_waitcnt lgkmcnt(0)
	v_readfirstlane_b32 s0, v108
	v_readfirstlane_b32 s1, v109
	s_add_u32 s0, s0, s22
	s_addc_u32 s1, s1, 0
	s_lshr_b32 s28, s16, 2
	s_and_b32 s31, s27, 3
.Lc1i_182:
	s_andn2_b64 vcc, exec, s[12:13]
	s_cbranch_vccnz .Lc1i_237
	s_and_b32 s0, s27, 8
	s_add_i32 s0, s0, 0x23f88
	v_mov_b32_e32 v108, s0
	s_lshr_b32 s12, s14, 3
	v_add_u32_e32 v108, 0, v108
	ds_read_b64 v[108:109], v108
	s_mov_b32 s29, 8
	s_mov_b64 s[14:15], 0x100
	s_mov_b32 s31, 0
	s_mov_b32 s28, s16
	s_waitcnt lgkmcnt(0)
	v_readfirstlane_b32 s0, v108
	v_readfirstlane_b32 s1, v109
	s_add_u32 s0, s0, s22
	s_addc_u32 s1, s1, 0
	s_add_i32 s30, s12, 1
	s_mov_b64 s[12:13], s[4:5]
	s_mov_b64 s[16:17], 0

.Lc1i_185:
	v_mov_b32_e32 v108, 0x23f80
	s_add_i32 s0, s27, 0xfffff000
	v_add_u32_e32 v108, 0, v108
	ds_read_b64 v[108:109], v108
	s_lshr_b32 s66, s0, 3
	s_mov_b32 s30, 3
	s_mov_b64 s[14:15], 0x400
	s_mov_b32 s29, 2
	s_waitcnt lgkmcnt(0)
	v_readfirstlane_b32 s1, v108
	v_readfirstlane_b32 s0, v109
	s_add_u32 s12, s1, s23
	s_addc_u32 s13, s0, 0
	s_lshl_b64 s[0:1], s[66:67], 20
	s_add_u32 s0, s12, s0
	s_addc_u32 s1, s13, s1
	s_lshl_b64 s[12:13], s[66:67], 18
	s_add_u32 s12, s19, s12
	s_addc_u32 s13, s20, s13
	s_bfe_u32 s28, s27, 0x10002
	s_and_b32 s31, s27, 3

.Lc1i_187:
	s_andn2_b64 vcc, exec, s[16:17]
	s_cbranch_vccnz .Lc1i_189
	s_ashr_i32 s14, s27, 11
	s_bfe_u32 s12, s27, 0x80003
	s_cmpk_lt_u32 s27, 0x800
	s_mov_b32 s0, 0x23f70
	s_cselect_b32 s0, s0, 0x23f78
	v_mov_b32_e32 v108, s0
	s_mov_b32 s31, 0
	v_add_u32_e32 v108, 0, v108
	ds_read_b64 v[108:109], v108
	s_mov_b32 s29, 8
	s_waitcnt lgkmcnt(0)
	v_readfirstlane_b32 s1, v108
	v_readfirstlane_b32 s0, v109
	s_add_u32 s1, s1, s23
	s_addc_u32 s13, s0, 0
	s_lshl_b32 s0, s12, 20
	s_add_u32 s0, s1, s0
	s_addc_u32 s1, s13, 0
	s_lshl_b32 s12, s12, 19
	s_add_u32 s12, s21, s12
	s_addc_u32 s13, s24, 0
	s_add_i32 s30, s14, 1
	s_and_b32 s28, s27, 7
	s_mov_b64 s[14:15], 0x100
.Lc1i_189:
	v_lshl_or_b32 v111, s28, 7, v176
	v_mad_u64_u32 v[108:109], s[16:17], s14, v111, 0
	v_mov_b32_e32 v110, v109
	v_mad_u64_u32 v[110:111], s[16:17], s15, v111, v[110:111]
	v_mov_b32_e32 v109, v110
	v_lshl_add_u64 v[108:109], v[108:109], 2, s[0:1]
	s_lshl_b32 s66, s31, 8
	v_lshl_add_u64 v[108:109], s[66:67], 2, v[108:109]
	v_lshl_add_u64 v[108:109], s[10:11], 2, v[108:109]
	v_lshlrev_b32_e32 v174, 2, v178
	v_lshl_add_u64 v[108:109], v[108:109], 0, v[174:175]
	s_lshl_b64 s[0:1], s[14:15], 2
	v_lshl_add_u64 v[110:111], v[108:109], 0, s[0:1]
	global_load_dwordx4 v[112:115], v[108:109], off nt
	global_load_dwordx4 v[116:119], v[110:111], off nt
	v_lshl_add_u64 v[108:109], v[110:111], 0, s[0:1]
	v_lshl_add_u64 v[110:111], v[108:109], 0, s[0:1]
	global_load_dwordx4 v[140:143], v[108:109], off nt
	global_load_dwordx4 v[144:147], v[110:111], off nt
	v_lshl_add_u64 v[108:109], v[110:111], 0, s[0:1]
	v_lshl_add_u64 v[110:111], v[108:109], 0, s[0:1]
	global_load_dwordx4 v[164:167], v[108:109], off nt
	global_load_dwordx4 v[168:171], v[110:111], off nt
	v_lshl_add_u64 v[108:109], v[110:111], 0, s[0:1]
	global_load_dwordx4 v[120:123], v[108:109], off nt
	v_lshl_add_u64 v[108:109], v[108:109], 0, s[0:1]
	global_load_dwordx4 v[148:151], v[108:109], off nt
	v_lshl_add_u64 v[108:109], v[108:109], 0, s[0:1]
	global_load_dwordx4 v[124:127], v[108:109], off nt
	v_lshl_add_u64 v[108:109], v[108:109], 0, s[0:1]
	global_load_dwordx4 v[152:155], v[108:109], off nt
	v_lshl_add_u64 v[108:109], v[108:109], 0, s[0:1]
	global_load_dwordx4 v[128:131], v[108:109], off nt
	v_lshl_add_u64 v[108:109], v[108:109], 0, s[0:1]
	global_load_dwordx4 v[156:159], v[108:109], off nt
	v_lshl_add_u64 v[108:109], v[108:109], 0, s[0:1]
	global_load_dwordx4 v[132:135], v[108:109], off nt
	v_lshl_add_u64 v[108:109], v[108:109], 0, s[0:1]
	s_waitcnt vmcnt(22)
	v_lshl_add_u64 v[136:137], v[108:109], 0, s[0:1]
	global_load_dwordx4 v[160:163], v[108:109], off nt
	s_add_i32 s16, s66, s10
	global_load_dwordx4 v[108:111], v[136:137], off nt
	v_lshl_add_u64 v[136:137], v[136:137], 0, s[0:1]
	global_load_dwordx4 v[136:139], v[136:137], off nt
	v_or_b32_e32 v181, s16, v178
	v_writelane_b32 v246, s12, 40
	v_writelane_b32 v246, s13, 41
	v_writelane_b32 v246, s16, 42
	v_writelane_b32 v246, s28, 43
	v_writelane_b32 v246, s29, 44
	v_writelane_b32 v246, s30, 45
	s_mov_b32 s26, 1
	v_writelane_b32 v246, s26, 49
	s_branch .Lc1_iskip

.Lc1_iskip:
	v_readlane_b32 s2, v246, 0
	v_readlane_b32 s3, v246, 1
	v_readlane_b32 s4, v246, 2
	v_readlane_b32 s5, v246, 3
	v_readlane_b32 s10, v246, 4
	v_readlane_b32 s11, v246, 5
	v_readlane_b32 s12, v246, 6
	v_readlane_b32 s13, v246, 7
	v_readlane_b32 s16, v246, 8
	v_readlane_b32 s17, v246, 9
	v_readlane_b32 s19, v246, 10
	v_readlane_b32 s20, v246, 11
	v_readlane_b32 s21, v246, 12
	v_readlane_b32 s22, v246, 13
	v_readlane_b32 s23, v246, 14
	v_readlane_b32 s24, v246, 15
	v_readlane_b32 s28, v246, 16
	v_readlane_b32 s29, v246, 17
	v_readlane_b32 s30, v246, 18
	v_readlane_b32 s31, v246, 19
	v_readlane_b32 s66, v246, 20
	s_nop 4
	v_mov_b32_e32 v37, s31
	ds_read2_b32 v[40:41], v57 offset1:1
	ds_read2_b32 v[44:45], v57 offset0:2 offset1:3
	ds_read2_b32 v[42:43], v57 offset0:4 offset1:5
	ds_read2_b32 v[38:39], v57 offset0:6 offset1:7
	ds_read_b128 v[18:21], v37 offset:16896
	ds_read_b128 v[22:25], v37 offset:16912
	ds_read_b128 v[82:85], v37 offset:8704
	ds_read_b128 v[86:89], v37 offset:8720
	s_mul_hi_i32 s0, s25, 0x3e0f83e1
	s_lshr_b32 s1, s0, 31
	s_ashr_i32 s45, s0, 5
	s_waitcnt lgkmcnt(1)
	v_fma_f32 v81, v40, v82, v18
	s_waitcnt lgkmcnt(0)
	v_fma_f32 v98, v40, v86, v22
	v_fma_f32 v99, v40, v83, v19
	v_fma_f32 v100, v40, v87, v23
	v_fma_f32 v20, v40, v84, v20
	v_fma_f32 v101, v40, v88, v24
	v_fmac_f32_e32 v21, v40, v85
	v_fmac_f32_e32 v25, v40, v89
	ds_read_b128 v[82:85], v37 offset:8976
	ds_read_b128 v[86:89], v37 offset:8960
	s_add_i32 s45, s45, s1
	s_mul_i32 s0, s45, 0xffffff7c
	s_add_i32 s44, s25, s0
	s_waitcnt lgkmcnt(1)
	v_fmac_f32_e32 v98, v41, v82
	s_waitcnt lgkmcnt(0)
	v_fmac_f32_e32 v81, v41, v86
	v_fmac_f32_e32 v99, v41, v87
	v_fmac_f32_e32 v100, v41, v83
	v_fmac_f32_e32 v20, v41, v88
	v_fmac_f32_e32 v101, v41, v84
	v_fmac_f32_e32 v21, v41, v89
	v_fmac_f32_e32 v25, v41, v85
	ds_read_b128 v[82:85], v37 offset:9232
	ds_read_b128 v[86:89], v37 offset:9216
	s_mul_i32 s0, s45, 0x318
	s_add_i32 s1, s21, s38
	s_add_i32 s26, s1, s0
	s_waitcnt lgkmcnt(1)
	v_fmac_f32_e32 v98, v44, v82
	s_waitcnt lgkmcnt(0)
	v_fmac_f32_e32 v81, v44, v86
	v_fmac_f32_e32 v99, v44, v87
	v_fmac_f32_e32 v100, v44, v83
	v_fmac_f32_e32 v20, v44, v88
	v_fmac_f32_e32 v101, v44, v84
	v_fmac_f32_e32 v21, v44, v89
	v_fmac_f32_e32 v25, v44, v85
	ds_read_b128 v[82:85], v37 offset:9488
	ds_read_b128 v[86:89], v37 offset:9472
	s_ashr_i32 s27, s26, 31
	s_lshl_b64 s[0:1], s[26:27], 13
	s_waitcnt lgkmcnt(1)
	v_fmac_f32_e32 v98, v45, v82
	s_waitcnt lgkmcnt(0)
	v_fmac_f32_e32 v81, v45, v86
	v_fmac_f32_e32 v99, v45, v87
	v_fmac_f32_e32 v100, v45, v83
	v_fmac_f32_e32 v20, v45, v88
	v_fmac_f32_e32 v101, v45, v84
	v_fmac_f32_e32 v21, v45, v89
	v_fmac_f32_e32 v25, v45, v85
	ds_read2_b32 v[18:19], v57 offset0:14 offset1:15
	ds_read2_b32 v[22:23], v57 offset0:12 offset1:13
	ds_read2_b32 v[40:41], v57 offset0:10 offset1:11
	ds_read2_b32 v[44:45], v57 offset0:8 offset1:9
	ds_read_b128 v[82:85], v37 offset:9728
	ds_read_b128 v[86:89], v37 offset:9744
	s_waitcnt lgkmcnt(1)
	v_fmac_f32_e32 v81, v42, v82
	s_waitcnt lgkmcnt(0)
	v_fmac_f32_e32 v98, v42, v86
	v_fmac_f32_e32 v99, v42, v83
	v_fmac_f32_e32 v100, v42, v87
	v_fmac_f32_e32 v20, v42, v84
	v_fmac_f32_e32 v101, v42, v88
	v_fmac_f32_e32 v21, v42, v85
	v_fmac_f32_e32 v25, v42, v89
	ds_read_b128 v[82:85], v37 offset:10000
	ds_read_b128 v[86:89], v37 offset:9984
	s_waitcnt lgkmcnt(1)
	v_fmac_f32_e32 v98, v43, v82
	s_waitcnt lgkmcnt(0)
	v_fmac_f32_e32 v81, v43, v86
	v_fmac_f32_e32 v99, v43, v87
	v_fmac_f32_e32 v100, v43, v83
	v_fmac_f32_e32 v20, v43, v88
	v_fmac_f32_e32 v101, v43, v84
	v_fmac_f32_e32 v21, v43, v89
	v_fmac_f32_e32 v25, v43, v85
	ds_read_b128 v[82:85], v37 offset:10256
	ds_read_b128 v[86:89], v37 offset:10240
	s_waitcnt lgkmcnt(1)
	v_fmac_f32_e32 v98, v38, v82
	s_waitcnt lgkmcnt(0)
	v_fmac_f32_e32 v81, v38, v86
	v_fmac_f32_e32 v99, v38, v87
	v_fmac_f32_e32 v100, v38, v83
	v_fmac_f32_e32 v20, v38, v88
	v_fmac_f32_e32 v101, v38, v84
	v_fmac_f32_e32 v21, v38, v89
	v_fmac_f32_e32 v25, v38, v85
	ds_read_b128 v[82:85], v37 offset:10512
	ds_read_b128 v[86:89], v37 offset:10496
	s_waitcnt lgkmcnt(1)
	v_fmac_f32_e32 v98, v39, v82
	s_waitcnt lgkmcnt(0)
	v_fmac_f32_e32 v81, v39, v86
	v_fmac_f32_e32 v99, v39, v87
	v_fmac_f32_e32 v100, v39, v83
	v_fmac_f32_e32 v20, v39, v88
	v_fmac_f32_e32 v101, v39, v84
	v_fmac_f32_e32 v21, v39, v89
	v_fmac_f32_e32 v25, v39, v85
	ds_read_b128 v[82:85], v37 offset:10752
	ds_read_b128 v[86:89], v37 offset:10768
	ds_read_b128 v[90:93], v37 offset:11024
	ds_read_b128 v[94:97], v37 offset:11008
	s_waitcnt lgkmcnt(3)
	v_mov_b32_e32 v24, v82
	s_waitcnt lgkmcnt(2)
	v_mov_b32_e32 v38, v89
	s_waitcnt lgkmcnt(1)
	v_mov_b32_e32 v39, v93
	v_pk_mul_f32 v[38:39], v[44:45], v[38:39]
	v_mov_b32_e32 v89, v92
	v_add_f32_e32 v38, v25, v38
	s_waitcnt lgkmcnt(0)
	v_mov_b32_e32 v25, v94
	v_pk_mul_f32 v[24:25], v[44:45], v[24:25]
	v_mov_b32_e32 v94, v83
	v_add_f32_e32 v24, v81, v24
	v_add_f32_e32 v81, v24, v25
	v_mov_b32_e32 v24, v86
	v_mov_b32_e32 v25, v90
	v_pk_mul_f32 v[24:25], v[44:45], v[24:25]
	v_mov_b32_e32 v90, v87
	v_add_f32_e32 v24, v98, v24
	v_add_f32_e32 v98, v25, v24
	v_pk_mul_f32 v[24:25], v[44:45], v[94:95]
	s_nop 0
	v_add_f32_e32 v24, v99, v24
	v_add_f32_e32 v94, v24, v25
	v_pk_mul_f32 v[24:25], v[44:45], v[90:91]
	s_nop 0
	v_add_f32_e32 v24, v100, v24
	v_add_f32_e32 v95, v25, v24
	v_mov_b32_e32 v24, v84
	v_mov_b32_e32 v25, v96
	v_pk_mul_f32 v[24:25], v[44:45], v[24:25]
	v_mov_b32_e32 v96, v85
	v_add_f32_e32 v20, v20, v24
	v_add_f32_e32 v99, v20, v25
	v_pk_mul_f32 v[24:25], v[44:45], v[88:89]
	s_nop 0
	v_add_f32_e32 v20, v101, v24
	v_add_f32_e32 v100, v25, v20
	v_pk_mul_f32 v[24:25], v[44:45], v[96:97]
	ds_read_b128 v[42:45], v37 offset:11280
	ds_read_b128 v[82:85], v37 offset:11264
	ds_read_b128 v[86:89], v37 offset:11536
	ds_read_b128 v[90:93], v37 offset:11520
	v_add_f32_e32 v20, v21, v24
	v_add_f32_e32 v96, v20, v25
	s_waitcnt lgkmcnt(3)
	v_mov_b32_e32 v20, v45
	s_waitcnt lgkmcnt(1)
	v_mov_b32_e32 v21, v89
	v_add_f32_e32 v24, v39, v38
	v_pk_mul_f32 v[20:21], v[40:41], v[20:21]
	s_waitcnt lgkmcnt(0)
	v_mov_b32_e32 v25, v90
	v_add_f32_e32 v20, v24, v20
	v_mov_b32_e32 v24, v82
	v_pk_mul_f32 v[24:25], v[40:41], v[24:25]
	v_mov_b32_e32 v90, v83
	v_add_f32_e32 v24, v81, v24
	v_add_f32_e32 v81, v24, v25
	v_mov_b32_e32 v24, v42
	v_mov_b32_e32 v25, v86
	v_pk_mul_f32 v[24:25], v[40:41], v[24:25]
	v_mov_b32_e32 v86, v43
	v_add_f32_e32 v24, v98, v24
	v_add_f32_e32 v97, v24, v25
	v_pk_mul_f32 v[24:25], v[40:41], v[90:91]
	v_mov_b32_e32 v45, v88
	v_add_f32_e32 v24, v94, v24
	v_add_f32_e32 v90, v24, v25
	v_pk_mul_f32 v[24:25], v[40:41], v[86:87]
	s_nop 0
	v_add_f32_e32 v24, v95, v24
	v_add_f32_e32 v91, v24, v25
	v_mov_b32_e32 v24, v84
	v_mov_b32_e32 v25, v92
	v_pk_mul_f32 v[24:25], v[40:41], v[24:25]
	v_mov_b32_e32 v92, v85
	v_add_f32_e32 v24, v99, v24
	v_add_f32_e32 v94, v24, v25
	v_pk_mul_f32 v[24:25], v[40:41], v[44:45]
	s_nop 0
	v_add_f32_e32 v24, v100, v24
	v_add_f32_e32 v95, v24, v25
	v_pk_mul_f32 v[24:25], v[40:41], v[92:93]
	ds_read_b128 v[38:41], v37 offset:11776
	ds_read_b128 v[42:45], v37 offset:11792
	ds_read_b128 v[82:85], v37 offset:12048
	ds_read_b128 v[86:89], v37 offset:12032
	v_add_f32_e32 v24, v96, v24
	v_add_f32_e32 v92, v24, v25
	v_add_f32_e32 v24, v20, v21
	s_waitcnt lgkmcnt(2)
	v_mov_b32_e32 v20, v45
	s_waitcnt lgkmcnt(1)
	v_mov_b32_e32 v21, v85
	v_pk_mul_f32 v[20:21], v[22:23], v[20:21]
	s_waitcnt lgkmcnt(0)
	v_mov_b32_e32 v25, v86
	v_add_f32_e32 v20, v24, v20
	v_mov_b32_e32 v24, v38
	v_pk_mul_f32 v[24:25], v[22:23], v[24:25]
	v_mov_b32_e32 v86, v39
	v_add_f32_e32 v24, v81, v24
	v_add_f32_e32 v81, v24, v25
	v_mov_b32_e32 v24, v42
	v_mov_b32_e32 v25, v82
	v_pk_mul_f32 v[24:25], v[22:23], v[24:25]
	v_mov_b32_e32 v82, v43
	v_add_f32_e32 v24, v97, v24
	v_add_f32_e32 v93, v25, v24
	v_pk_mul_f32 v[24:25], v[22:23], v[86:87]
	v_mov_b32_e32 v45, v84
	v_add_f32_e32 v24, v90, v24
	v_add_f32_e32 v90, v24, v25
	v_pk_mul_f32 v[24:25], v[22:23], v[82:83]
	v_add_f32_e32 v82, v21, v20
	v_add_f32_e32 v24, v91, v24
	v_add_f32_e32 v91, v25, v24
	v_mov_b32_e32 v24, v40
	v_mov_b32_e32 v25, v88
	v_pk_mul_f32 v[24:25], v[22:23], v[24:25]
	v_mov_b32_e32 v88, v41
	v_add_f32_e32 v24, v94, v24
	v_add_f32_e32 v94, v24, v25
	v_pk_mul_f32 v[24:25], v[22:23], v[44:45]
	v_pk_mul_f32 v[22:23], v[22:23], v[88:89]
	v_add_f32_e32 v24, v95, v24
	v_add_f32_e32 v22, v92, v22
	v_add_f32_e32 v88, v22, v23
	ds_read_b128 v[20:23], v37 offset:12304
	ds_read_b128 v[38:41], v37 offset:12288
	ds_read_b128 v[42:45], v37 offset:12560
	v_add_f32_e32 v95, v25, v24
	s_waitcnt lgkmcnt(2)
	v_mov_b32_e32 v24, v23
	s_waitcnt lgkmcnt(1)
	v_mov_b32_e32 v86, v38
	s_waitcnt lgkmcnt(0)
	v_mov_b32_e32 v25, v45
	v_pk_mul_f32 v[24:25], v[18:19], v[24:25]
	s_nop 0
	v_add_f32_e32 v24, v82, v24
	ds_read_b128 v[82:85], v37 offset:12544
	s_waitcnt lgkmcnt(0)
	v_mov_b32_e32 v87, v82
	v_pk_mul_f32 v[86:87], v[18:19], v[86:87]
	v_mov_b32_e32 v82, v39
	v_add_f32_e32 v23, v81, v86
	v_add_f32_e32 v45, v23, v87
	v_mov_b32_e32 v86, v20
	v_mov_b32_e32 v87, v42
	v_pk_mul_f32 v[86:87], v[18:19], v[86:87]
	v_pk_mul_f32 v[38:39], v[18:19], v[82:83]
	v_add_f32_e32 v20, v93, v86
	v_add_f32_e32 v81, v20, v87
	v_add_f32_e32 v20, v90, v38
	v_mov_b32_e32 v42, v21
	v_add_f32_e32 v38, v20, v39
	v_pk_mul_f32 v[20:21], v[18:19], v[42:43]
	v_mov_b32_e32 v23, v44
	v_add_f32_e32 v20, v91, v20
	v_add_f32_e32 v39, v20, v21
	v_mov_b32_e32 v20, v40
	v_mov_b32_e32 v21, v84
	v_pk_mul_f32 v[20:21], v[18:19], v[20:21]
	v_mov_b32_e32 v84, v41
	v_add_f32_e32 v20, v94, v20
	v_add_f32_e32 v40, v20, v21
	v_pk_mul_f32 v[20:21], v[18:19], v[22:23]
	v_pk_mul_f32 v[18:19], v[18:19], v[84:85]
	v_add_f32_e32 v20, v95, v20
	v_add_f32_e32 v18, v88, v18
	v_add_f32_e32 v23, v20, v21
	v_add_f32_e32 v21, v18, v19
	v_mul_f32_e32 v18, 0xbfb8aa3b, v45
	v_exp_f32_e32 v18, v18
	v_add_f32_e32 v22, v24, v25
	v_mul_f32_e32 v21, 0xbfb8aa3b, v21
	v_exp_f32_e32 v21, v21
	v_add_f32_e32 v18, 1.0, v18
	v_cmp_gt_f32_e32 vcc, s93, v18
	v_mul_f32_e32 v23, 0xbfb8aa3b, v23
	v_add_f32_e32 v21, 1.0, v21
	v_cndmask_b32_e64 v19, 0, 32, vcc
	v_ldexp_f32 v18, v18, v19
	v_log_f32_e32 v18, v18
	v_exp_f32_e32 v23, v23
	v_mul_f32_e32 v22, 0xbfb8aa3b, v22
	v_exp_f32_e32 v22, v22
	v_mul_f32_e32 v19, 0x3f317217, v18
	v_fma_f32 v19, v18, s62, -v19
	v_fmac_f32_e32 v19, 0x3377d1cf, v18
	v_fmac_f32_e32 v19, 0x3f317217, v18
	v_cmp_lt_f32_e64 s[14:15], |v18|, s63
	v_add_f32_e32 v23, 1.0, v23
	v_add_f32_e32 v22, 1.0, v22
	v_cndmask_b32_e64 v18, v18, v19, s[14:15]
	v_cndmask_b32_e32 v19, 0, v243, vcc
	v_sub_f32_e32 v18, v18, v19
	v_mul_f32_e32 v19, 0xbfb8aa3b, v38
	v_exp_f32_e32 v19, v19
	s_nop 0
	v_add_f32_e32 v19, 1.0, v19
	v_cmp_gt_f32_e32 vcc, s93, v19
	s_nop 1
	v_cndmask_b32_e64 v20, 0, 32, vcc
	v_ldexp_f32 v19, v19, v20
	v_log_f32_e32 v19, v19
	s_nop 0
	v_mul_f32_e32 v20, 0x3f317217, v19
	v_fma_f32 v20, v19, s62, -v20
	v_fmac_f32_e32 v20, 0x3377d1cf, v19
	v_fmac_f32_e32 v20, 0x3f317217, v19
	v_cmp_lt_f32_e64 s[14:15], |v19|, s63
	s_nop 1
	v_cndmask_b32_e64 v19, v19, v20, s[14:15]
	v_cndmask_b32_e32 v20, 0, v243, vcc
	v_sub_f32_e32 v19, v19, v20
	v_mul_f32_e32 v20, 0xbfb8aa3b, v40
	v_exp_f32_e32 v20, v20
	v_pk_mul_f32 v[18:19], v[18:19], s[76:77] op_sel_hi:[1,0]
	v_add_f32_e32 v20, 1.0, v20
	v_cmp_gt_f32_e32 vcc, s93, v20
	v_cvt_pk_bf16_f32 v18, v18, v19
	s_nop 0
	v_cndmask_b32_e64 v24, 0, 32, vcc
	v_ldexp_f32 v20, v20, v24
	v_log_f32_e32 v20, v20
	s_nop 0
	v_mul_f32_e32 v24, 0x3f317217, v20
	v_fma_f32 v24, v20, s62, -v24
	v_fmac_f32_e32 v24, 0x3377d1cf, v20
	v_fmac_f32_e32 v24, 0x3f317217, v20
	v_cmp_lt_f32_e64 s[14:15], |v20|, s63
	s_nop 1
	v_cndmask_b32_e64 v20, v20, v24, s[14:15]
	v_cndmask_b32_e32 v24, 0, v243, vcc
	v_cmp_gt_f32_e32 vcc, s93, v21
	v_sub_f32_e32 v20, v20, v24
	s_nop 0
	v_cndmask_b32_e64 v24, 0, 32, vcc
	v_ldexp_f32 v21, v21, v24
	v_log_f32_e32 v21, v21
	s_nop 0
	v_mul_f32_e32 v24, 0x3f317217, v21
	v_fma_f32 v24, v21, s62, -v24
	v_fmac_f32_e32 v24, 0x3377d1cf, v21
	v_fmac_f32_e32 v24, 0x3f317217, v21
	v_cmp_lt_f32_e64 s[14:15], |v21|, s63
	s_nop 1
	v_cndmask_b32_e64 v21, v21, v24, s[14:15]
	v_cndmask_b32_e32 v24, 0, v243, vcc
	v_sub_f32_e32 v21, v21, v24
	v_mul_f32_e32 v24, 0xbfb8aa3b, v81
	v_exp_f32_e32 v24, v24
	v_pk_mul_f32 v[20:21], v[20:21], s[76:77] op_sel_hi:[1,0]
	v_add_f32_e32 v24, 1.0, v24
	v_cmp_gt_f32_e32 vcc, s93, v24
	v_cvt_pk_bf16_f32 v19, v20, v21
	s_nop 0
	v_cndmask_b32_e64 v25, 0, 32, vcc
	v_ldexp_f32 v24, v24, v25
	v_log_f32_e32 v24, v24
	s_nop 0
	v_mul_f32_e32 v25, 0x3f317217, v24
	v_fma_f32 v25, v24, s62, -v25
	v_fmac_f32_e32 v25, 0x3377d1cf, v24
	v_fmac_f32_e32 v25, 0x3f317217, v24
	v_cmp_lt_f32_e64 s[14:15], |v24|, s63
	s_nop 1
	v_cndmask_b32_e64 v24, v24, v25, s[14:15]
	v_cndmask_b32_e32 v25, 0, v243, vcc
	v_sub_f32_e32 v24, v24, v25
	v_mul_f32_e32 v25, 0xbfb8aa3b, v39
	v_exp_f32_e32 v25, v25
	s_nop 0
	v_add_f32_e32 v25, 1.0, v25
	v_cmp_gt_f32_e32 vcc, s93, v25
	s_nop 1
	v_cndmask_b32_e64 v38, 0, 32, vcc
	v_ldexp_f32 v25, v25, v38
	v_log_f32_e32 v25, v25
	s_nop 0
	v_mul_f32_e32 v38, 0x3f317217, v25
	v_fma_f32 v38, v25, s62, -v38
	v_fmac_f32_e32 v38, 0x3377d1cf, v25
	v_fmac_f32_e32 v38, 0x3f317217, v25
	v_cmp_lt_f32_e64 s[14:15], |v25|, s63
	s_nop 1
	v_cndmask_b32_e64 v25, v25, v38, s[14:15]
	v_cndmask_b32_e32 v38, 0, v243, vcc
	v_cmp_gt_f32_e32 vcc, s93, v23
	v_sub_f32_e32 v25, v25, v38
	v_pk_mul_f32 v[24:25], v[24:25], s[76:77] op_sel_hi:[1,0]
	v_cndmask_b32_e64 v38, 0, 32, vcc
	v_ldexp_f32 v23, v23, v38
	v_log_f32_e32 v23, v23
	v_cvt_pk_bf16_f32 v20, v24, v25
	v_lshlrev_b32_e32 v24, 16, v18
	v_and_b32_e32 v25, 0xffff0000, v18
	v_mul_f32_e32 v38, 0x3f317217, v23
	v_fma_f32 v38, v23, s62, -v38
	v_fmac_f32_e32 v38, 0x3377d1cf, v23
	v_fmac_f32_e32 v38, 0x3f317217, v23
	v_cmp_lt_f32_e64 s[14:15], |v23|, s63
	v_lshlrev_b32_e32 v40, 16, v20
	v_and_b32_e32 v41, 0xffff0000, v20
	v_cndmask_b32_e64 v23, v23, v38, s[14:15]
	v_cndmask_b32_e32 v38, 0, v243, vcc
	v_cmp_gt_f32_e32 vcc, s93, v22
	v_sub_f32_e32 v38, v23, v38
	s_nop 0
	v_cndmask_b32_e64 v23, 0, 32, vcc
	v_ldexp_f32 v22, v22, v23
	v_log_f32_e32 v22, v22
	s_nop 0
	v_mul_f32_e32 v23, 0x3f317217, v22
	v_fma_f32 v23, v22, s62, -v23
	v_fmac_f32_e32 v23, 0x3377d1cf, v22
	v_fmac_f32_e32 v23, 0x3f317217, v22
	v_cmp_lt_f32_e64 s[14:15], |v22|, s63
	s_nop 1
	v_cndmask_b32_e64 v22, v22, v23, s[14:15]
	v_cndmask_b32_e32 v23, 0, v243, vcc
	v_sub_f32_e32 v39, v22, v23
	v_pk_mul_f32 v[22:23], v[38:39], s[76:77] op_sel_hi:[1,0]
	v_lshlrev_b32_e32 v38, 16, v19
	v_cvt_pk_bf16_f32 v21, v22, v23
	v_lshl_add_u64 v[22:23], v[26:27], 0, s[0:1]
	global_store_dwordx4 v[22:23], v[18:21], off
	v_and_b32_e32 v39, 0xffff0000, v19
	v_lshlrev_b32_e32 v42, 16, v21
	v_add_f32_dpp v18, v24, v24 row_shr:1 row_mask:0xf bank_mask:0xf bound_ctrl:1
	v_mov_b32_e32 v19, v69
	v_and_b32_e32 v43, 0xffff0000, v21
	v_add_f32_dpp v18, v18, v18 row_shr:2 row_mask:0xf bank_mask:0xf bound_ctrl:1
	s_add_i32 s0, s26, 1
	s_ashr_i32 s1, s0, 31
	v_add_f32_dpp v18, v18, v18 row_shr:4 row_mask:0xf bank_mask:0xf bound_ctrl:1
	s_lshl_b64 s[0:1], s[0:1], 13
	s_nop 0
	v_add_f32_dpp v18, v18, v18 row_shr:8 row_mask:0xf bank_mask:0xf bound_ctrl:1
	s_nop 1
	v_mov_b32_dpp v19, v18 row_bcast:15 row_mask:0xa bank_mask:0xf bound_ctrl:1
	v_add_f32_e32 v18, v18, v19
	v_mov_b32_e32 v19, v69
	s_nop 1
	v_mov_b32_dpp v19, v18 row_bcast:31 row_mask:0xc bank_mask:0xf bound_ctrl:1
	v_add_f32_e32 v88, v18, v19
	v_add_f32_dpp v18, v25, v25 row_shr:1 row_mask:0xf bank_mask:0xf bound_ctrl:1
	v_mov_b32_e32 v19, v69
	v_readlane_b32 s27, v88, 63
	v_add_f32_dpp v18, v18, v18 row_shr:2 row_mask:0xf bank_mask:0xf bound_ctrl:1
	s_nop 1
	v_add_f32_dpp v18, v18, v18 row_shr:4 row_mask:0xf bank_mask:0xf bound_ctrl:1
	s_nop 1
	v_add_f32_dpp v18, v18, v18 row_shr:8 row_mask:0xf bank_mask:0xf bound_ctrl:1
	s_nop 1
	v_mov_b32_dpp v19, v18 row_bcast:15 row_mask:0xa bank_mask:0xf bound_ctrl:1
	v_add_f32_e32 v18, v18, v19
	v_mov_b32_e32 v19, v69
	s_nop 1
	v_mov_b32_dpp v19, v18 row_bcast:31 row_mask:0xc bank_mask:0xf bound_ctrl:1
	v_add_f32_e32 v87, v18, v19
	v_add_f32_dpp v18, v38, v38 row_shr:1 row_mask:0xf bank_mask:0xf bound_ctrl:1
	v_mov_b32_e32 v19, v69
	v_add_u32_e32 v38, 0x1100, v57
	v_add_f32_dpp v18, v18, v18 row_shr:2 row_mask:0xf bank_mask:0xf bound_ctrl:1
	v_readlane_b32 s48, v87, 63
	s_nop 0
	v_add_f32_dpp v18, v18, v18 row_shr:4 row_mask:0xf bank_mask:0xf bound_ctrl:1
	s_nop 1
	v_add_f32_dpp v18, v18, v18 row_shr:8 row_mask:0xf bank_mask:0xf bound_ctrl:1
	s_nop 1
	v_mov_b32_dpp v19, v18 row_bcast:15 row_mask:0xa bank_mask:0xf bound_ctrl:1
	v_add_f32_e32 v18, v18, v19
	v_mov_b32_e32 v19, v69
	s_nop 1
	v_mov_b32_dpp v19, v18 row_bcast:31 row_mask:0xc bank_mask:0xf bound_ctrl:1
	v_add_f32_e32 v86, v18, v19
	v_add_f32_dpp v18, v39, v39 row_shr:1 row_mask:0xf bank_mask:0xf bound_ctrl:1
	v_mov_b32_e32 v19, v69
	v_readlane_b32 s50, v86, 63
	v_add_f32_dpp v18, v18, v18 row_shr:2 row_mask:0xf bank_mask:0xf bound_ctrl:1
	s_nop 1
	v_add_f32_dpp v18, v18, v18 row_shr:4 row_mask:0xf bank_mask:0xf bound_ctrl:1
	s_nop 1
	v_add_f32_dpp v18, v18, v18 row_shr:8 row_mask:0xf bank_mask:0xf bound_ctrl:1
	s_nop 1
	v_mov_b32_dpp v19, v18 row_bcast:15 row_mask:0xa bank_mask:0xf bound_ctrl:1
	v_add_f32_e32 v18, v18, v19
	v_mov_b32_e32 v19, v69
	s_nop 1
	v_mov_b32_dpp v19, v18 row_bcast:31 row_mask:0xc bank_mask:0xf bound_ctrl:1
	v_add_f32_e32 v85, v18, v19
	v_add_f32_dpp v18, v40, v40 row_shr:1 row_mask:0xf bank_mask:0xf bound_ctrl:1
	v_mov_b32_e32 v19, v69
	v_add_u32_e32 v40, 0x1108, v57
	v_add_f32_dpp v18, v18, v18 row_shr:2 row_mask:0xf bank_mask:0xf bound_ctrl:1
	v_readlane_b32 s56, v85, 63
	s_nop 0
	v_add_f32_dpp v18, v18, v18 row_shr:4 row_mask:0xf bank_mask:0xf bound_ctrl:1
	s_nop 1
	v_add_f32_dpp v18, v18, v18 row_shr:8 row_mask:0xf bank_mask:0xf bound_ctrl:1
	s_nop 1
	v_mov_b32_dpp v19, v18 row_bcast:15 row_mask:0xa bank_mask:0xf bound_ctrl:1
	v_add_f32_e32 v18, v18, v19
	v_mov_b32_e32 v19, v69
	s_nop 1
	v_mov_b32_dpp v19, v18 row_bcast:31 row_mask:0xc bank_mask:0xf bound_ctrl:1
	v_add_f32_e32 v84, v18, v19
	v_add_f32_dpp v18, v41, v41 row_shr:1 row_mask:0xf bank_mask:0xf bound_ctrl:1
	v_mov_b32_e32 v19, v69
	v_readlane_b32 s49, v84, 63
	v_add_f32_dpp v18, v18, v18 row_shr:2 row_mask:0xf bank_mask:0xf bound_ctrl:1
	s_nop 1
	v_add_f32_dpp v18, v18, v18 row_shr:4 row_mask:0xf bank_mask:0xf bound_ctrl:1
	s_nop 1
	v_add_f32_dpp v18, v18, v18 row_shr:8 row_mask:0xf bank_mask:0xf bound_ctrl:1
	s_nop 1
	v_mov_b32_dpp v19, v18 row_bcast:15 row_mask:0xa bank_mask:0xf bound_ctrl:1
	v_add_f32_e32 v18, v18, v19
	v_mov_b32_e32 v19, v69
	s_nop 1
	v_mov_b32_dpp v19, v18 row_bcast:31 row_mask:0xc bank_mask:0xf bound_ctrl:1
	v_add_f32_e32 v83, v18, v19
	v_add_f32_dpp v18, v42, v42 row_shr:1 row_mask:0xf bank_mask:0xf bound_ctrl:1
	v_mov_b32_e32 v19, v69
	v_readlane_b32 s51, v83, 63
	v_add_f32_dpp v18, v18, v18 row_shr:2 row_mask:0xf bank_mask:0xf bound_ctrl:1
	s_nop 1
	v_add_f32_dpp v18, v18, v18 row_shr:4 row_mask:0xf bank_mask:0xf bound_ctrl:1
	s_nop 1
	v_add_f32_dpp v18, v18, v18 row_shr:8 row_mask:0xf bank_mask:0xf bound_ctrl:1
	s_nop 1
	v_mov_b32_dpp v19, v18 row_bcast:15 row_mask:0xa bank_mask:0xf bound_ctrl:1
	v_add_f32_e32 v18, v18, v19
	v_mov_b32_e32 v19, v69
	s_nop 1
	v_mov_b32_dpp v19, v18 row_bcast:31 row_mask:0xc bank_mask:0xf bound_ctrl:1
	v_add_f32_e32 v82, v18, v19
	v_add_f32_dpp v18, v43, v43 row_shr:1 row_mask:0xf bank_mask:0xf bound_ctrl:1
	v_mov_b32_e32 v19, v69
	v_readlane_b32 s57, v82, 63
	v_add_f32_dpp v18, v18, v18 row_shr:2 row_mask:0xf bank_mask:0xf bound_ctrl:1
	s_nop 1
	v_add_f32_dpp v18, v18, v18 row_shr:4 row_mask:0xf bank_mask:0xf bound_ctrl:1
	s_nop 1
	v_add_f32_dpp v18, v18, v18 row_shr:8 row_mask:0xf bank_mask:0xf bound_ctrl:1
	s_nop 1
	v_mov_b32_dpp v19, v18 row_bcast:15 row_mask:0xa bank_mask:0xf bound_ctrl:1
	v_add_f32_e32 v18, v18, v19
	v_mov_b32_e32 v19, v69
	s_nop 1
	v_mov_b32_dpp v19, v18 row_bcast:31 row_mask:0xc bank_mask:0xf bound_ctrl:1
	v_add_f32_e32 v81, v18, v19
	ds_read_b128 v[90:93], v37 offset:12800
	ds_read_b128 v[94:97], v37 offset:12816
	ds_read_b128 v[22:25], v37 offset:17168
	ds_read_b128 v[18:21], v37 offset:17152
	ds_read2_b32 v[38:39], v38 offset1:1
	ds_read2_b32 v[44:45], v40 offset1:1
	v_add_u32_e32 v40, 0x1110, v57
	ds_read2_b32 v[42:43], v40 offset1:1
	v_add_u32_e32 v40, 0x1118, v57
	ds_read2_b32 v[40:41], v40 offset1:1
	s_waitcnt lgkmcnt(3)
	v_fma_f32 v89, v90, v38, v18
	v_fma_f32 v104, v94, v38, v22
	v_fma_f32 v105, v91, v38, v19
	v_fma_f32 v106, v95, v38, v23
	v_fma_f32 v20, v92, v38, v20
	v_fma_f32 v107, v96, v38, v24
	v_fmac_f32_e32 v21, v93, v38
	v_fmac_f32_e32 v25, v97, v38
	ds_read_b128 v[90:93], v37 offset:13072
	ds_read_b128 v[94:97], v37 offset:13056
	v_add_u32_e32 v18, 0x1138, v57
	v_add_u32_e32 v22, 0x1130, v57
	v_add_u32_e32 v24, 0x1128, v57
	s_waitcnt lgkmcnt(1)
	v_fmac_f32_e32 v104, v39, v90
	s_waitcnt lgkmcnt(0)
	v_fmac_f32_e32 v89, v39, v94
	v_fmac_f32_e32 v105, v39, v95
	v_fmac_f32_e32 v106, v39, v91
	v_fmac_f32_e32 v20, v39, v96
	v_fmac_f32_e32 v107, v39, v92
	v_fmac_f32_e32 v21, v39, v97
	v_fmac_f32_e32 v25, v39, v93
	ds_read_b128 v[90:93], v37 offset:13328
	ds_read_b128 v[94:97], v37 offset:13312
	v_readlane_b32 s70, v81, 63
	s_waitcnt lgkmcnt(1)
	v_fmac_f32_e32 v104, v44, v90
	s_waitcnt lgkmcnt(0)
	v_fmac_f32_e32 v89, v44, v94
	v_fmac_f32_e32 v105, v44, v95
	v_fmac_f32_e32 v106, v44, v91
	v_fmac_f32_e32 v20, v44, v96
	v_fmac_f32_e32 v107, v44, v92
	v_fmac_f32_e32 v21, v44, v97
	v_fmac_f32_e32 v25, v44, v93
	ds_read_b128 v[90:93], v37 offset:13584
	ds_read_b128 v[94:97], v37 offset:13568
	ds_read2_b32 v[18:19], v18 offset1:1
	ds_read2_b32 v[22:23], v22 offset1:1
	ds_read2_b32 v[38:39], v24 offset1:1
	v_add_u32_e32 v24, 0x1120, v57
	s_waitcnt lgkmcnt(3)
	v_fmac_f32_e32 v89, v45, v94
	v_fmac_f32_e32 v104, v45, v90
	v_fmac_f32_e32 v105, v45, v95
	v_fmac_f32_e32 v106, v45, v91
	v_fmac_f32_e32 v20, v45, v96
	v_fmac_f32_e32 v107, v45, v92
	v_fmac_f32_e32 v21, v45, v97
	v_fmac_f32_e32 v25, v45, v93
	ds_read2_b32 v[44:45], v24 offset1:1
	ds_read_b128 v[90:93], v37 offset:13824
	ds_read_b128 v[94:97], v37 offset:13840
	s_waitcnt lgkmcnt(1)
	v_fmac_f32_e32 v89, v42, v90
	s_waitcnt lgkmcnt(0)
	v_fmac_f32_e32 v104, v42, v94
	v_fmac_f32_e32 v105, v42, v91
	v_fmac_f32_e32 v106, v42, v95
	v_fmac_f32_e32 v20, v42, v92
	v_fmac_f32_e32 v107, v42, v96
	v_fmac_f32_e32 v21, v42, v93
	v_fmac_f32_e32 v25, v42, v97
	ds_read_b128 v[90:93], v37 offset:14096
	ds_read_b128 v[94:97], v37 offset:14080
	s_waitcnt lgkmcnt(1)
	v_fmac_f32_e32 v104, v43, v90
	s_waitcnt lgkmcnt(0)
	v_fmac_f32_e32 v89, v43, v94
	v_fmac_f32_e32 v105, v43, v95
	v_fmac_f32_e32 v106, v43, v91
	v_fmac_f32_e32 v20, v43, v96
	v_fmac_f32_e32 v107, v43, v92
	v_fmac_f32_e32 v21, v43, v97
	v_fmac_f32_e32 v25, v43, v93
	ds_read_b128 v[90:93], v37 offset:14352
	ds_read_b128 v[94:97], v37 offset:14336
	s_waitcnt lgkmcnt(1)
	v_fmac_f32_e32 v104, v40, v90
	s_waitcnt lgkmcnt(0)
	v_fmac_f32_e32 v89, v40, v94
	v_fmac_f32_e32 v105, v40, v95
	v_fmac_f32_e32 v106, v40, v91
	v_fmac_f32_e32 v20, v40, v96
	v_fmac_f32_e32 v107, v40, v92
	v_fmac_f32_e32 v21, v40, v97
	v_fmac_f32_e32 v25, v40, v93
	ds_read_b128 v[90:93], v37 offset:14608
	ds_read_b128 v[94:97], v37 offset:14592
	s_waitcnt lgkmcnt(1)
	v_fmac_f32_e32 v104, v41, v90
	s_waitcnt lgkmcnt(0)
	v_fmac_f32_e32 v89, v41, v94
	v_fmac_f32_e32 v105, v41, v95
	v_fmac_f32_e32 v106, v41, v91
	v_fmac_f32_e32 v20, v41, v96
	v_fmac_f32_e32 v107, v41, v92
	v_fmac_f32_e32 v21, v41, v97
	v_fmac_f32_e32 v25, v41, v93
	ds_read_b128 v[40:43], v37 offset:14848
	ds_read_b128 v[90:93], v37 offset:14864
	ds_read_b128 v[94:97], v37 offset:15120
	s_waitcnt lgkmcnt(2)
	v_mov_b32_e32 v24, v40
	s_waitcnt lgkmcnt(1)
	v_mov_b32_e32 v98, v93
	s_waitcnt lgkmcnt(0)
	v_mov_b32_e32 v99, v97
	v_pk_mul_f32 v[102:103], v[44:45], v[98:99]
	ds_read_b128 v[98:101], v37 offset:15104
	v_add_f32_e32 v97, v25, v102
	v_mov_b32_e32 v93, v96
	s_waitcnt lgkmcnt(0)
	v_mov_b32_e32 v25, v98
	v_pk_mul_f32 v[24:25], v[44:45], v[24:25]
	v_mov_b32_e32 v98, v41
	v_add_f32_e32 v24, v89, v24
	v_add_f32_e32 v89, v24, v25
	v_mov_b32_e32 v24, v90
	v_mov_b32_e32 v25, v94
	v_pk_mul_f32 v[24:25], v[44:45], v[24:25]
	v_mov_b32_e32 v94, v91
	v_add_f32_e32 v24, v104, v24
	v_add_f32_e32 v102, v25, v24
	v_pk_mul_f32 v[24:25], v[44:45], v[98:99]
	s_nop 0
	v_add_f32_e32 v24, v105, v24
	v_add_f32_e32 v104, v24, v25
	v_pk_mul_f32 v[24:25], v[44:45], v[94:95]
	s_nop 0
	v_add_f32_e32 v24, v106, v24
	v_add_f32_e32 v105, v25, v24
	v_mov_b32_e32 v24, v42
	v_mov_b32_e32 v25, v100
	v_pk_mul_f32 v[24:25], v[44:45], v[24:25]
	v_mov_b32_e32 v100, v43
	v_add_f32_e32 v20, v20, v24
	v_add_f32_e32 v106, v20, v25
	v_pk_mul_f32 v[24:25], v[44:45], v[92:93]
	s_nop 0
	v_add_f32_e32 v20, v107, v24
	v_add_f32_e32 v107, v25, v20
	v_pk_mul_f32 v[24:25], v[44:45], v[100:101]
	s_nop 0
	v_add_f32_e32 v20, v21, v24
	v_add_f32_e32 v24, v103, v97
	ds_read_b128 v[40:43], v37 offset:15376
	ds_read_b128 v[90:93], v37 offset:15360
	ds_read_b128 v[94:97], v37 offset:15632
	ds_read_b128 v[98:101], v37 offset:15616
	v_add_f32_e32 v44, v20, v25
	s_waitcnt lgkmcnt(3)
	v_mov_b32_e32 v20, v43
	s_waitcnt lgkmcnt(1)
	v_mov_b32_e32 v21, v97
	v_pk_mul_f32 v[20:21], v[38:39], v[20:21]
	s_waitcnt lgkmcnt(0)
	v_mov_b32_e32 v25, v98
	v_add_f32_e32 v20, v24, v20
	v_mov_b32_e32 v24, v90
	v_pk_mul_f32 v[24:25], v[38:39], v[24:25]
	v_mov_b32_e32 v98, v91
	v_add_f32_e32 v24, v89, v24
	v_add_f32_e32 v89, v24, v25
	v_mov_b32_e32 v24, v40
	v_mov_b32_e32 v25, v94
	v_pk_mul_f32 v[24:25], v[38:39], v[24:25]
	v_mov_b32_e32 v94, v41
	v_add_f32_e32 v24, v102, v24
	v_add_f32_e32 v102, v24, v25
	v_pk_mul_f32 v[24:25], v[38:39], v[98:99]
	v_mov_b32_e32 v43, v96
	v_add_f32_e32 v24, v104, v24
	v_add_f32_e32 v98, v24, v25
	v_pk_mul_f32 v[24:25], v[38:39], v[94:95]
	s_nop 0
	v_add_f32_e32 v24, v105, v24
	v_add_f32_e32 v99, v24, v25
	v_mov_b32_e32 v24, v92
	v_mov_b32_e32 v25, v100
	v_pk_mul_f32 v[24:25], v[38:39], v[24:25]
	v_mov_b32_e32 v100, v93
	v_add_f32_e32 v24, v106, v24
	v_add_f32_e32 v103, v24, v25
	v_pk_mul_f32 v[24:25], v[38:39], v[42:43]
	s_nop 0
	v_add_f32_e32 v24, v107, v24
	v_add_f32_e32 v104, v24, v25
	v_pk_mul_f32 v[24:25], v[38:39], v[100:101]
	s_nop 0
	v_add_f32_e32 v24, v44, v24
	ds_read_b128 v[38:41], v37 offset:15872
	ds_read_b128 v[42:45], v37 offset:15888
	ds_read_b128 v[90:93], v37 offset:16144
	ds_read_b128 v[94:97], v37 offset:16128
	v_add_f32_e32 v100, v24, v25
	v_add_f32_e32 v24, v20, v21
	s_waitcnt lgkmcnt(2)
	v_mov_b32_e32 v20, v45
	s_waitcnt lgkmcnt(1)
	v_mov_b32_e32 v21, v93
	v_pk_mul_f32 v[20:21], v[22:23], v[20:21]
	s_waitcnt lgkmcnt(0)
	v_mov_b32_e32 v25, v94
	v_add_f32_e32 v20, v24, v20
	v_mov_b32_e32 v24, v38
	v_pk_mul_f32 v[24:25], v[22:23], v[24:25]
	v_mov_b32_e32 v94, v39
	v_add_f32_e32 v24, v89, v24
	v_add_f32_e32 v89, v24, v25
	v_mov_b32_e32 v24, v42
	v_mov_b32_e32 v25, v90
	v_pk_mul_f32 v[24:25], v[22:23], v[24:25]
	v_mov_b32_e32 v90, v43
	v_add_f32_e32 v24, v102, v24
	v_add_f32_e32 v101, v25, v24
	v_pk_mul_f32 v[24:25], v[22:23], v[94:95]
	v_mov_b32_e32 v45, v92
	v_add_f32_e32 v24, v98, v24
	v_add_f32_e32 v98, v24, v25
	v_pk_mul_f32 v[24:25], v[22:23], v[90:91]
	v_add_f32_e32 v90, v21, v20
	v_add_f32_e32 v24, v99, v24
	v_add_f32_e32 v99, v25, v24
	v_mov_b32_e32 v24, v40
	v_mov_b32_e32 v25, v96
	v_pk_mul_f32 v[24:25], v[22:23], v[24:25]
	v_mov_b32_e32 v96, v41
	v_add_f32_e32 v24, v103, v24
	v_add_f32_e32 v102, v24, v25
	v_pk_mul_f32 v[24:25], v[22:23], v[44:45]
	v_pk_mul_f32 v[22:23], v[22:23], v[96:97]
	v_add_f32_e32 v24, v104, v24
	v_add_f32_e32 v22, v100, v22
	v_add_f32_e32 v96, v22, v23
	ds_read_b128 v[20:23], v37 offset:16400
	ds_read_b128 v[38:41], v37 offset:16384
	ds_read_b128 v[42:45], v37 offset:16656
	v_add_f32_e32 v103, v25, v24
	s_waitcnt lgkmcnt(2)
	v_mov_b32_e32 v24, v23
	s_waitcnt lgkmcnt(1)
	v_mov_b32_e32 v94, v38
	s_waitcnt lgkmcnt(0)
	v_mov_b32_e32 v25, v45
	v_pk_mul_f32 v[24:25], v[18:19], v[24:25]
	s_nop 0
	v_add_f32_e32 v24, v90, v24
	ds_read_b128 v[90:93], v37 offset:16640
	s_waitcnt lgkmcnt(0)
	v_mov_b32_e32 v95, v90
	v_pk_mul_f32 v[94:95], v[18:19], v[94:95]
	v_mov_b32_e32 v90, v39
	v_add_f32_e32 v23, v89, v94
	v_add_f32_e32 v37, v23, v95
	v_mov_b32_e32 v94, v20
	v_mov_b32_e32 v95, v42
	v_pk_mul_f32 v[94:95], v[18:19], v[94:95]
	v_pk_mul_f32 v[38:39], v[18:19], v[90:91]
	v_add_f32_e32 v20, v101, v94
	v_add_f32_e32 v45, v20, v95
	v_add_f32_e32 v20, v98, v38
	v_mov_b32_e32 v42, v21
	v_add_f32_e32 v38, v20, v39
	v_pk_mul_f32 v[20:21], v[18:19], v[42:43]
	v_mov_b32_e32 v23, v44
	v_add_f32_e32 v20, v99, v20
	v_add_f32_e32 v39, v20, v21
	v_mov_b32_e32 v20, v40
	v_mov_b32_e32 v21, v92
	v_pk_mul_f32 v[20:21], v[18:19], v[20:21]
	v_mov_b32_e32 v92, v41
	v_add_f32_e32 v20, v102, v20
	v_add_f32_e32 v40, v20, v21
	v_pk_mul_f32 v[20:21], v[18:19], v[22:23]
	v_pk_mul_f32 v[18:19], v[18:19], v[92:93]
	v_add_f32_e32 v20, v103, v20
	v_add_f32_e32 v18, v96, v18
	v_add_f32_e32 v23, v20, v21
	v_add_f32_e32 v21, v18, v19
	v_mul_f32_e32 v18, 0xbfb8aa3b, v37
	v_exp_f32_e32 v18, v18
	v_add_f32_e32 v22, v24, v25
	v_mul_f32_e32 v21, 0xbfb8aa3b, v21
	v_exp_f32_e32 v21, v21
	v_add_f32_e32 v18, 1.0, v18
	v_cmp_gt_f32_e32 vcc, s93, v18
	v_mul_f32_e32 v23, 0xbfb8aa3b, v23
	v_add_f32_e32 v21, 1.0, v21
	v_cndmask_b32_e64 v19, 0, 32, vcc
	v_ldexp_f32 v18, v18, v19
	v_log_f32_e32 v18, v18
	v_exp_f32_e32 v23, v23
	v_mul_f32_e32 v22, 0xbfb8aa3b, v22
	v_exp_f32_e32 v22, v22
	v_mul_f32_e32 v19, 0x3f317217, v18
	v_fma_f32 v19, v18, s62, -v19
	v_fmac_f32_e32 v19, 0x3377d1cf, v18
	v_fmac_f32_e32 v19, 0x3f317217, v18
	v_cmp_lt_f32_e64 s[14:15], |v18|, s63
	v_add_f32_e32 v23, 1.0, v23
	v_add_f32_e32 v22, 1.0, v22
	v_cndmask_b32_e64 v18, v18, v19, s[14:15]
	v_cndmask_b32_e32 v19, 0, v243, vcc
	v_sub_f32_e32 v18, v18, v19
	v_mul_f32_e32 v19, 0xbfb8aa3b, v38
	v_exp_f32_e32 v19, v19
	s_nop 0
	v_add_f32_e32 v19, 1.0, v19
	v_cmp_gt_f32_e32 vcc, s93, v19
	s_nop 1
	v_cndmask_b32_e64 v20, 0, 32, vcc
	v_ldexp_f32 v19, v19, v20
	v_log_f32_e32 v19, v19
	s_nop 0
	v_mul_f32_e32 v20, 0x3f317217, v19
	v_fma_f32 v20, v19, s62, -v20
	v_fmac_f32_e32 v20, 0x3377d1cf, v19
	v_fmac_f32_e32 v20, 0x3f317217, v19
	v_cmp_lt_f32_e64 s[14:15], |v19|, s63
	s_nop 1
	v_cndmask_b32_e64 v19, v19, v20, s[14:15]
	v_cndmask_b32_e32 v20, 0, v243, vcc
	v_sub_f32_e32 v19, v19, v20
	v_mul_f32_e32 v20, 0xbfb8aa3b, v40
	v_exp_f32_e32 v20, v20
	v_pk_mul_f32 v[18:19], v[18:19], s[76:77] op_sel_hi:[1,0]
	v_add_f32_e32 v20, 1.0, v20
	v_cmp_gt_f32_e32 vcc, s93, v20
	v_cvt_pk_bf16_f32 v18, v18, v19
	s_nop 0
	v_cndmask_b32_e64 v24, 0, 32, vcc
	v_ldexp_f32 v20, v20, v24
	v_log_f32_e32 v20, v20
	s_nop 0
	v_mul_f32_e32 v24, 0x3f317217, v20
	v_fma_f32 v24, v20, s62, -v24
	v_fmac_f32_e32 v24, 0x3377d1cf, v20
	v_fmac_f32_e32 v24, 0x3f317217, v20
	v_cmp_lt_f32_e64 s[14:15], |v20|, s63
	s_nop 1
	v_cndmask_b32_e64 v20, v20, v24, s[14:15]
	v_cndmask_b32_e32 v24, 0, v243, vcc
	v_cmp_gt_f32_e32 vcc, s93, v21
	v_sub_f32_e32 v20, v20, v24
	s_nop 0
	v_cndmask_b32_e64 v24, 0, 32, vcc
	v_ldexp_f32 v21, v21, v24
	v_log_f32_e32 v21, v21
	s_nop 0
	v_mul_f32_e32 v24, 0x3f317217, v21
	v_fma_f32 v24, v21, s62, -v24
	v_fmac_f32_e32 v24, 0x3377d1cf, v21
	v_fmac_f32_e32 v24, 0x3f317217, v21
	v_cmp_lt_f32_e64 s[14:15], |v21|, s63
	s_nop 1
	v_cndmask_b32_e64 v21, v21, v24, s[14:15]
	v_cndmask_b32_e32 v24, 0, v243, vcc
	v_sub_f32_e32 v21, v21, v24
	v_mul_f32_e32 v24, 0xbfb8aa3b, v45
	v_exp_f32_e32 v24, v24
	v_pk_mul_f32 v[20:21], v[20:21], s[76:77] op_sel_hi:[1,0]
	v_sub_f32_e32 v45, s27, v88
	v_cvt_pk_bf16_f32 v19, v20, v21
	v_add_f32_e32 v24, 1.0, v24
	v_cmp_gt_f32_e32 vcc, s93, v24
	v_mul_f32_e32 v45, 0x3fb8aa3b, v45
	v_exp_f32_e32 v45, v45
	v_cndmask_b32_e64 v25, 0, 32, vcc
	v_ldexp_f32 v24, v24, v25
	v_log_f32_e32 v24, v24
	s_nop 0
	v_mul_f32_e32 v25, 0x3f317217, v24
	v_fma_f32 v25, v24, s62, -v25
	v_fmac_f32_e32 v25, 0x3377d1cf, v24
	v_fmac_f32_e32 v25, 0x3f317217, v24
	v_cmp_lt_f32_e64 s[14:15], |v24|, s63
	s_nop 1
	v_cndmask_b32_e64 v24, v24, v25, s[14:15]
	v_cndmask_b32_e32 v25, 0, v243, vcc
	v_sub_f32_e32 v24, v24, v25
	v_mul_f32_e32 v25, 0xbfb8aa3b, v39
	v_exp_f32_e32 v25, v25
	s_nop 0
	v_add_f32_e32 v25, 1.0, v25
	v_cmp_gt_f32_e32 vcc, s93, v25
	s_nop 1
	v_cndmask_b32_e64 v37, 0, 32, vcc
	v_ldexp_f32 v25, v25, v37
	v_log_f32_e32 v25, v25
	s_nop 0
	v_mul_f32_e32 v37, 0x3f317217, v25
	v_fma_f32 v37, v25, s62, -v37
	v_fmac_f32_e32 v37, 0x3377d1cf, v25
	v_fmac_f32_e32 v37, 0x3f317217, v25
	v_cmp_lt_f32_e64 s[14:15], |v25|, s63
	s_nop 1
	v_cndmask_b32_e64 v25, v25, v37, s[14:15]
	v_cndmask_b32_e32 v37, 0, v243, vcc
	v_cmp_gt_f32_e32 vcc, s93, v23
	v_sub_f32_e32 v25, v25, v37
	v_pk_mul_f32 v[24:25], v[24:25], s[76:77] op_sel_hi:[1,0]
	v_cndmask_b32_e64 v37, 0, 32, vcc
	v_ldexp_f32 v23, v23, v37
	v_log_f32_e32 v23, v23
	v_cvt_pk_bf16_f32 v20, v24, v25
	v_lshlrev_b32_e32 v24, 16, v18
	v_and_b32_e32 v25, 0xffff0000, v18
	v_mul_f32_e32 v37, 0x3f317217, v23
	v_fma_f32 v37, v23, s62, -v37
	v_fmac_f32_e32 v37, 0x3377d1cf, v23
	v_fmac_f32_e32 v37, 0x3f317217, v23
	v_cmp_lt_f32_e64 s[14:15], |v23|, s63
	v_and_b32_e32 v40, 0xffff0000, v20
	s_nop 0
	v_cndmask_b32_e64 v23, v23, v37, s[14:15]
	v_cndmask_b32_e32 v37, 0, v243, vcc
	v_cmp_gt_f32_e32 vcc, s93, v22
	v_sub_f32_e32 v38, v23, v37
	v_lshlrev_b32_e32 v37, 16, v19
	v_cndmask_b32_e64 v23, 0, 32, vcc
	v_ldexp_f32 v22, v22, v23
	v_log_f32_e32 v22, v22
	s_nop 0
	v_mul_f32_e32 v23, 0x3f317217, v22
	v_fma_f32 v23, v22, s62, -v23
	v_fmac_f32_e32 v23, 0x3377d1cf, v22
	v_fmac_f32_e32 v23, 0x3f317217, v22
	v_cmp_lt_f32_e64 s[14:15], |v22|, s63
	s_nop 1
	v_cndmask_b32_e64 v22, v22, v23, s[14:15]
	v_cndmask_b32_e32 v23, 0, v243, vcc
	v_sub_f32_e32 v39, v22, v23
	v_pk_mul_f32 v[22:23], v[38:39], s[76:77] op_sel_hi:[1,0]
	v_and_b32_e32 v38, 0xffff0000, v19
	v_cvt_pk_bf16_f32 v21, v22, v23
	v_lshl_add_u64 v[22:23], v[26:27], 0, s[0:1]
	global_store_dwordx4 v[22:23], v[18:21], off
	v_lshlrev_b32_e32 v39, 16, v20
	v_lshlrev_b32_e32 v41, 16, v21
	v_add_f32_dpp v18, v24, v24 row_shr:1 row_mask:0xf bank_mask:0xf bound_ctrl:1
	v_mov_b32_e32 v19, v69
	v_and_b32_e32 v42, 0xffff0000, v21
	v_add_f32_dpp v18, v18, v18 row_shr:2 row_mask:0xf bank_mask:0xf bound_ctrl:1
	s_nop 1
	v_add_f32_dpp v18, v18, v18 row_shr:4 row_mask:0xf bank_mask:0xf bound_ctrl:1
	s_nop 1
	v_add_f32_dpp v18, v18, v18 row_shr:8 row_mask:0xf bank_mask:0xf bound_ctrl:1
	s_nop 1
	v_mov_b32_dpp v19, v18 row_bcast:15 row_mask:0xa bank_mask:0xf bound_ctrl:1
	v_add_f32_e32 v18, v18, v19
	v_mov_b32_e32 v19, v69
	s_nop 1
	v_mov_b32_dpp v19, v18 row_bcast:31 row_mask:0xc bank_mask:0xf bound_ctrl:1
	v_add_f32_e32 v18, v18, v19
	v_mov_b32_e32 v19, v69
	v_readlane_b32 s14, v18, 63
	s_nop 1
	v_sub_f32_e32 v18, s14, v18
	v_add_f32_e32 v22, v18, v24
	v_sub_f32_e32 v22, s14, v22
	v_add_f32_dpp v18, v25, v25 row_shr:1 row_mask:0xf bank_mask:0xf bound_ctrl:1
	v_mul_f32_e32 v22, 0x3fb8aa3b, v22
	v_exp_f32_e32 v22, v22
	v_add_f32_dpp v18, v18, v18 row_shr:2 row_mask:0xf bank_mask:0xf bound_ctrl:1
	s_nop 1
	v_add_f32_dpp v18, v18, v18 row_shr:4 row_mask:0xf bank_mask:0xf bound_ctrl:1
	s_nop 1
	v_add_f32_dpp v18, v18, v18 row_shr:8 row_mask:0xf bank_mask:0xf bound_ctrl:1
	s_nop 1
	v_mov_b32_dpp v19, v18 row_bcast:15 row_mask:0xa bank_mask:0xf bound_ctrl:1
	v_add_f32_e32 v18, v18, v19
	v_mov_b32_e32 v19, v69
	s_nop 1
	v_mov_b32_dpp v19, v18 row_bcast:31 row_mask:0xc bank_mask:0xf bound_ctrl:1
	v_add_f32_e32 v18, v18, v19
	v_mov_b32_e32 v19, v69
	v_readlane_b32 s15, v18, 63
	s_nop 1
	v_sub_f32_e32 v18, s15, v18
	v_add_f32_e32 v23, v18, v25
	s_nop 0
	v_add_f32_dpp v18, v37, v37 row_shr:1 row_mask:0xf bank_mask:0xf bound_ctrl:1
	s_nop 1
	v_add_f32_dpp v18, v18, v18 row_shr:2 row_mask:0xf bank_mask:0xf bound_ctrl:1
	s_nop 1
	v_add_f32_dpp v18, v18, v18 row_shr:4 row_mask:0xf bank_mask:0xf bound_ctrl:1
	s_nop 1
	v_add_f32_dpp v18, v18, v18 row_shr:8 row_mask:0xf bank_mask:0xf bound_ctrl:1
	s_nop 1
	v_mov_b32_dpp v19, v18 row_bcast:15 row_mask:0xa bank_mask:0xf bound_ctrl:1
	v_add_f32_e32 v18, v18, v19
	v_mov_b32_e32 v19, v69
	s_nop 1
	v_mov_b32_dpp v19, v18 row_bcast:31 row_mask:0xc bank_mask:0xf bound_ctrl:1
	v_add_f32_e32 v18, v18, v19
	v_mov_b32_e32 v19, v69
	v_readlane_b32 s26, v18, 63
	s_nop 1
	v_sub_f32_e32 v18, s26, v18
	v_add_f32_e32 v24, v18, v37
	s_nop 0
	v_add_f32_dpp v18, v38, v38 row_shr:1 row_mask:0xf bank_mask:0xf bound_ctrl:1
	s_nop 1
	v_add_f32_dpp v18, v18, v18 row_shr:2 row_mask:0xf bank_mask:0xf bound_ctrl:1
	s_nop 1
	v_add_f32_dpp v18, v18, v18 row_shr:4 row_mask:0xf bank_mask:0xf bound_ctrl:1
	s_nop 1
	v_add_f32_dpp v18, v18, v18 row_shr:8 row_mask:0xf bank_mask:0xf bound_ctrl:1
	s_nop 1
	v_mov_b32_dpp v19, v18 row_bcast:15 row_mask:0xa bank_mask:0xf bound_ctrl:1
	v_add_f32_e32 v18, v18, v19
	v_mov_b32_e32 v19, v69
	s_nop 1
	v_mov_b32_dpp v19, v18 row_bcast:31 row_mask:0xc bank_mask:0xf bound_ctrl:1
	v_add_f32_e32 v18, v18, v19
	v_mov_b32_e32 v19, v69
	v_readlane_b32 s65, v18, 63
	s_nop 1
	v_sub_f32_e32 v18, s65, v18
	v_add_f32_e32 v25, v18, v38
	s_nop 0
	v_add_f32_dpp v18, v39, v39 row_shr:1 row_mask:0xf bank_mask:0xf bound_ctrl:1
	s_nop 1
	v_add_f32_dpp v18, v18, v18 row_shr:2 row_mask:0xf bank_mask:0xf bound_ctrl:1
	s_nop 1
	v_add_f32_dpp v18, v18, v18 row_shr:4 row_mask:0xf bank_mask:0xf bound_ctrl:1
	s_nop 1
	v_add_f32_dpp v18, v18, v18 row_shr:8 row_mask:0xf bank_mask:0xf bound_ctrl:1
	s_nop 1
	v_mov_b32_dpp v19, v18 row_bcast:15 row_mask:0xa bank_mask:0xf bound_ctrl:1
	v_add_f32_e32 v18, v18, v19
	v_mov_b32_e32 v19, v69
	s_nop 1
	v_mov_b32_dpp v19, v18 row_bcast:31 row_mask:0xc bank_mask:0xf bound_ctrl:1
	v_add_f32_e32 v18, v18, v19
	v_mov_b32_e32 v19, v69
	v_readlane_b32 s69, v18, 63
	s_nop 1
	v_sub_f32_e32 v18, s69, v18
	v_add_f32_e32 v37, v18, v39
	s_nop 0
	v_add_f32_dpp v18, v40, v40 row_shr:1 row_mask:0xf bank_mask:0xf bound_ctrl:1
	s_nop 1
	v_add_f32_dpp v18, v18, v18 row_shr:2 row_mask:0xf bank_mask:0xf bound_ctrl:1
	s_nop 1
	v_add_f32_dpp v18, v18, v18 row_shr:4 row_mask:0xf bank_mask:0xf bound_ctrl:1
	s_nop 1
	v_add_f32_dpp v18, v18, v18 row_shr:8 row_mask:0xf bank_mask:0xf bound_ctrl:1
	s_nop 1
	v_mov_b32_dpp v19, v18 row_bcast:15 row_mask:0xa bank_mask:0xf bound_ctrl:1
	v_add_f32_e32 v18, v18, v19
	v_mov_b32_e32 v19, v69
	s_nop 1
	v_mov_b32_dpp v19, v18 row_bcast:31 row_mask:0xc bank_mask:0xf bound_ctrl:1
	v_add_f32_e32 v18, v18, v19
	v_mov_b32_e32 v19, v69
	v_readlane_b32 s71, v18, 63
	s_nop 1
	v_sub_f32_e32 v18, s71, v18
	v_add_f32_e32 v38, v18, v40
	s_nop 0
	v_add_f32_dpp v18, v41, v41 row_shr:1 row_mask:0xf bank_mask:0xf bound_ctrl:1
	s_nop 1
	v_add_f32_dpp v18, v18, v18 row_shr:2 row_mask:0xf bank_mask:0xf bound_ctrl:1
	s_nop 1
	v_add_f32_dpp v18, v18, v18 row_shr:4 row_mask:0xf bank_mask:0xf bound_ctrl:1
	s_nop 1
	v_add_f32_dpp v18, v18, v18 row_shr:8 row_mask:0xf bank_mask:0xf bound_ctrl:1
	s_nop 1
	v_mov_b32_dpp v19, v18 row_bcast:15 row_mask:0xa bank_mask:0xf bound_ctrl:1
	v_add_f32_e32 v18, v18, v19
	v_mov_b32_e32 v19, v69
	s_nop 1
	v_mov_b32_dpp v19, v18 row_bcast:31 row_mask:0xc bank_mask:0xf bound_ctrl:1
	v_add_f32_e32 v18, v18, v19
	v_mov_b32_e32 v19, v69
	v_readlane_b32 s74, v18, 63
	s_nop 1
	v_sub_f32_e32 v18, s74, v18
	v_add_f32_e32 v39, v18, v41
	s_nop 0
	v_add_f32_dpp v18, v42, v42 row_shr:1 row_mask:0xf bank_mask:0xf bound_ctrl:1
	s_nop 1
	v_add_f32_dpp v18, v18, v18 row_shr:2 row_mask:0xf bank_mask:0xf bound_ctrl:1
	s_nop 1
	v_add_f32_dpp v18, v18, v18 row_shr:4 row_mask:0xf bank_mask:0xf bound_ctrl:1
	s_nop 1
	v_add_f32_dpp v18, v18, v18 row_shr:8 row_mask:0xf bank_mask:0xf bound_ctrl:1
	s_nop 1
	v_mov_b32_dpp v19, v18 row_bcast:15 row_mask:0xa bank_mask:0xf bound_ctrl:1
	v_add_f32_e32 v18, v18, v19
	v_mov_b32_e32 v19, v69
	s_nop 1
	v_mov_b32_dpp v19, v18 row_bcast:31 row_mask:0xc bank_mask:0xf bound_ctrl:1
	v_add_f32_e32 v18, v18, v19
	s_nop 0
	v_readlane_b32 s75, v18, 63
	s_nop 1
	v_sub_f32_e32 v18, s75, v18
	v_add_f32_e32 v40, v18, v42
	ds_read_b128 v[18:21], v58
	s_waitcnt lgkmcnt(0)
	v_lshlrev_b32_e32 v41, 16, v18
	v_mul_f32_e32 v22, v22, v41
	v_cvt_pk_bf16_f32 v22, v22, s0
	ds_write_b16 v59, v22 offset:26624
	v_sub_f32_e32 v22, s48, v87
	v_mul_f32_e32 v22, 0x3fb8aa3b, v22
	v_exp_f32_e32 v22, v22
	v_and_b32_e32 v18, 0xffff0000, v18
	v_lshlrev_b32_e32 v42, 16, v19
	v_and_b32_e32 v19, 0xffff0000, v19
	v_mul_f32_e32 v22, v22, v18
	v_cvt_pk_bf16_f32 v22, v22, s0
	ds_write_b16 v59, v22 offset:17552
	v_sub_f32_e32 v22, s15, v23
	v_mul_f32_e32 v22, 0x3fb8aa3b, v22
	v_exp_f32_e32 v22, v22
	v_lshlrev_b32_e32 v43, 16, v20
	v_and_b32_e32 v20, 0xffff0000, v20
	v_lshlrev_b32_e32 v44, 16, v21
	v_mul_f32_e32 v18, v22, v18
	v_cvt_pk_bf16_f32 v18, v18, s0
	ds_write_b16 v59, v18 offset:26768
	v_sub_f32_e32 v18, s50, v86
	v_mul_f32_e32 v18, 0x3fb8aa3b, v18
	v_exp_f32_e32 v18, v18
	v_and_b32_e32 v21, 0xffff0000, v21
	v_mul_f32_e32 v45, v45, v41
	v_cvt_pk_bf16_f32 v45, v45, s0
	v_mul_f32_e32 v18, v18, v42
	v_cvt_pk_bf16_f32 v18, v18, s0
	ds_write_b16 v59, v18 offset:17696
	v_sub_f32_e32 v18, s26, v24
	v_mul_f32_e32 v18, 0x3fb8aa3b, v18
	v_exp_f32_e32 v18, v18
	ds_write_b16 v59, v45 offset:17408
	v_mul_f32_e32 v18, v18, v42
	v_cvt_pk_bf16_f32 v18, v18, s0
	ds_write_b16 v59, v18 offset:26912
	v_sub_f32_e32 v18, s56, v85
	v_mul_f32_e32 v18, 0x3fb8aa3b, v18
	v_exp_f32_e32 v18, v18
	s_nop 0
	v_mul_f32_e32 v18, v18, v19
	v_cvt_pk_bf16_f32 v18, v18, s0
	ds_write_b16 v59, v18 offset:17840
	v_sub_f32_e32 v18, s65, v25
	v_mul_f32_e32 v18, 0x3fb8aa3b, v18
	v_exp_f32_e32 v18, v18
	s_nop 0
	v_mul_f32_e32 v18, v18, v19
	v_cvt_pk_bf16_f32 v18, v18, s0
	ds_write_b16 v59, v18 offset:27056
	v_sub_f32_e32 v18, s49, v84
	v_mul_f32_e32 v18, 0x3fb8aa3b, v18
	v_exp_f32_e32 v18, v18
	s_nop 0
	v_mul_f32_e32 v18, v18, v43
	v_cvt_pk_bf16_f32 v18, v18, s0
	ds_write_b16 v59, v18 offset:17984
	v_sub_f32_e32 v18, s69, v37
	v_mul_f32_e32 v18, 0x3fb8aa3b, v18
	v_exp_f32_e32 v18, v18
	s_nop 0
	v_mul_f32_e32 v18, v18, v43
	v_cvt_pk_bf16_f32 v18, v18, s0
	ds_write_b16 v59, v18 offset:27200
	v_sub_f32_e32 v18, s51, v83
	v_mul_f32_e32 v18, 0x3fb8aa3b, v18
	v_exp_f32_e32 v18, v18
	s_nop 0
	v_mul_f32_e32 v18, v18, v20
	v_cvt_pk_bf16_f32 v18, v18, s0
	ds_write_b16 v59, v18 offset:18128
	v_sub_f32_e32 v18, s71, v38
	v_mul_f32_e32 v18, 0x3fb8aa3b, v18
	v_exp_f32_e32 v18, v18
	s_nop 0
	v_mul_f32_e32 v18, v18, v20
	v_cvt_pk_bf16_f32 v18, v18, s0
	ds_write_b16 v59, v18 offset:27344
	v_sub_f32_e32 v18, s57, v82
	v_mul_f32_e32 v18, 0x3fb8aa3b, v18
	v_exp_f32_e32 v18, v18
	s_nop 0
	v_mul_f32_e32 v18, v18, v44
	v_cvt_pk_bf16_f32 v18, v18, s0
	ds_write_b16 v59, v18 offset:18272
	v_sub_f32_e32 v18, s74, v39
	v_mul_f32_e32 v18, 0x3fb8aa3b, v18
	v_exp_f32_e32 v18, v18
	s_nop 0
	v_mul_f32_e32 v18, v18, v44
	v_cvt_pk_bf16_f32 v18, v18, s0
	ds_write_b16 v59, v18 offset:27488
	v_sub_f32_e32 v18, s70, v81
	v_mul_f32_e32 v18, 0x3fb8aa3b, v18
	v_exp_f32_e32 v18, v18
	s_nop 0
	v_mul_f32_e32 v18, v18, v21
	v_cvt_pk_bf16_f32 v18, v18, s0
	ds_write_b16 v59, v18 offset:18416
	v_sub_f32_e32 v18, s75, v40
	v_mul_f32_e32 v18, 0x3fb8aa3b, v18
	v_exp_f32_e32 v18, v18
	s_nop 0
	v_mul_f32_e32 v18, v18, v21
	v_cvt_pk_bf16_f32 v18, v18, s0
	ds_write_b16 v59, v18 offset:27632
	s_and_saveexec_b64 s[0:1], s[4:5]
	s_cbranch_execz .LBB0_503
	s_cmp_gt_i32 s44, 3
	s_cselect_b32 s36, 0x87, 3
	s_mul_i32 s64, s45, 0x39c
	s_add_i32 s77, s21, s25
	s_add_i32 s78, s77, s64
	s_mul_i32 s64, s45, 0x4a4
	v_mul_f32_e32 v19, s14, v244
	v_mul_f32_e32 v20, s15, v244
	v_mul_f32_e32 v21, s26, v244
	s_add_i32 s36, s36, s64
	s_add_i32 s64, s21, s39
	v_mul_f32_e32 v18, s27, v244
	v_exp_f32_e32 v22, v19
	v_mul_f32_e32 v19, s48, v244
	v_exp_f32_e32 v23, v20
	v_mul_f32_e32 v20, s50, v244
	v_exp_f32_e32 v24, v21
	v_mul_f32_e32 v21, s56, v244
	s_add_i32 s36, s64, s36
	s_ashr_i32 s79, s78, 31
	v_exp_f32_e32 v18, v18
	v_exp_f32_e32 v19, v19
	v_exp_f32_e32 v20, v20
	v_exp_f32_e32 v21, v21
	s_add_i32 s80, s36, 0x84
	s_lshl_b64 s[78:79], s[78:79], 8
	s_add_u32 s78, s34, s78
	s_addc_u32 s79, s35, s79
	global_store_dwordx4 v69, v[18:21], s[78:79]
	s_ashr_i32 s81, s80, 31
	s_lshl_b64 s[80:81], s[80:81], 8
	v_mul_f32_e32 v18, s65, v244
	v_exp_f32_e32 v25, v18
	s_add_u32 s80, s34, s80
	s_addc_u32 s81, s35, s81
	v_mul_f32_e32 v19, s69, v244
	v_mul_f32_e32 v20, s71, v244
	v_mul_f32_e32 v21, s74, v244
	global_store_dwordx4 v69, v[22:25], s[80:81]
	v_mul_f32_e32 v18, s49, v244
	v_exp_f32_e32 v18, v18
	v_exp_f32_e32 v22, v19
	v_mul_f32_e32 v19, s51, v244
	v_exp_f32_e32 v23, v20
	v_mul_f32_e32 v20, s57, v244
	v_exp_f32_e32 v24, v21
	v_mul_f32_e32 v21, s70, v244
	v_exp_f32_e32 v19, v19
	v_exp_f32_e32 v20, v20
	v_exp_f32_e32 v21, v21
	global_store_dwordx4 v69, v[18:21], s[78:79] offset:16
	s_nop 1
	v_mul_f32_e32 v18, s75, v244
	v_exp_f32_e32 v25, v18
	global_store_dwordx4 v69, v[22:25], s[80:81] offset:16

.LBB0_874:
	s_or_b64 exec, exec, s[2:3]
	v_mov_b32_e32 v34, v0
	s_mov_b64 s[6:7], s[42:43]
	s_mov_b32 s11, s95
	s_mov_b32 s10, s85
	s_waitcnt lgkmcnt(0)
	v_mov_b32_e32 v2, 0x23f50
	s_barrier
	s_mov_b32 s25, s67
	v_add_u32_e32 v2, 0, v2
	ds_read_b64 v[2:3], v2
	s_lshl_b64 s[0:1], s[24:25], 12
	v_and_b32_e32 v38, 63, v34
	v_lshlrev_b32_e32 v30, 6, v38
	v_mov_b32_e32 v18, 0x23f58
	s_waitcnt lgkmcnt(0)
	v_readfirstlane_b32 s2, v2
	v_readfirstlane_b32 s3, v3
	s_add_u32 s2, s2, s0
	s_addc_u32 s3, s3, s1
	s_nop 2
	global_load_dwordx4 v[2:5], v30, s[2:3] offset:48
	global_load_dwordx4 v[6:9], v30, s[2:3] offset:32
	global_load_dwordx4 v[10:13], v30, s[2:3] offset:16
	global_load_dwordx4 v[14:17], v30, s[2:3]
	s_mul_i32 s77, s24, 0x1e000
	v_add_u32_e32 v18, 0, v18
	ds_read_b64 v[18:19], v18
	v_readfirstlane_b32 s12, v34
	s_waitcnt lgkmcnt(0)
	v_readfirstlane_b32 s3, v18
	v_readfirstlane_b32 s2, v19
	s_add_u32 s0, s3, s0
	s_addc_u32 s1, s2, s1
	global_load_dwordx4 v[18:21], v30, s[0:1] offset:48
	global_load_dwordx4 v[22:25], v30, s[0:1] offset:32
	global_load_dwordx4 v[26:29], v30, s[0:1] offset:16
	s_nop 0
	global_load_dwordx4 v[30:33], v30, s[0:1]
	s_movk_i32 s0, 0x3c00
	v_cmp_gt_i32_e32 vcc, s0, v34
	s_barrier
	s_and_saveexec_b64 s[2:3], vcc
	s_cbranch_execz .LBB0_882
	s_add_u32 s0, s6, s77
	s_addc_u32 s1, s7, 0
	s_add_u32 s0, s0, 0x12000
	s_addc_u32 s1, s1, 0
	v_lshrrev_b32_e32 v124, 8, v34
	v_and_b32_e32 v125, 0xff, v34
	v_lshlrev_b32_e32 v126, 4, v125
	v_and_b32_e32 v127, 3, v125
	v_lshlrev_b32_e32 v127, 10, v127
	v_lshrrev_b32_e32 v128, 2, v125
	v_lshlrev_b32_e32 v128, 4, v128
	v_add_u32_e32 v127, v127, v128
	v_add_u32_e32 v127, 0x8000, v127
	v_add_u32_e32 v129, 0, v124
	v_mul_u32_u24_e32 v130, 11, v129
	v_lshrrev_b32_e32 v130, 5, v130
	v_mul_u32_u24_e32 v164, 0x3000, v130
	v_lshl_add_u32 v164, v129, 12, v164
	v_add_u32_e32 v164, v164, v126
	global_load_dwordx4 v[132:135], v164, s[0:1]
	v_lshl_add_u32 v172, v129, 12, v127
	v_add_u32_e32 v129, 2, v124
	v_mul_u32_u24_e32 v130, 11, v129
	v_lshrrev_b32_e32 v130, 5, v130
	v_mul_u32_u24_e32 v165, 0x3000, v130
	v_lshl_add_u32 v165, v129, 12, v165
	v_add_u32_e32 v165, v165, v126
	global_load_dwordx4 v[136:139], v165, s[0:1]
	v_lshl_add_u32 v173, v129, 12, v127
	v_add_u32_e32 v129, 4, v124
	v_mul_u32_u24_e32 v130, 11, v129
	v_lshrrev_b32_e32 v130, 5, v130
	v_mul_u32_u24_e32 v166, 0x3000, v130
	v_lshl_add_u32 v166, v129, 12, v166
	v_add_u32_e32 v166, v166, v126
	global_load_dwordx4 v[140:143], v166, s[0:1]
	v_lshl_add_u32 v174, v129, 12, v127
	v_add_u32_e32 v129, 6, v124
	v_mul_u32_u24_e32 v130, 11, v129
	v_lshrrev_b32_e32 v130, 5, v130
	v_mul_u32_u24_e32 v167, 0x3000, v130
	v_lshl_add_u32 v167, v129, 12, v167
	v_add_u32_e32 v167, v167, v126
	global_load_dwordx4 v[144:147], v167, s[0:1]
	v_lshl_add_u32 v175, v129, 12, v127
	v_add_u32_e32 v129, 8, v124
	v_mul_u32_u24_e32 v130, 11, v129
	v_lshrrev_b32_e32 v130, 5, v130
	v_mul_u32_u24_e32 v168, 0x3000, v130
	v_lshl_add_u32 v168, v129, 12, v168
	v_add_u32_e32 v168, v168, v126
	global_load_dwordx4 v[148:151], v168, s[0:1]
	v_lshl_add_u32 v176, v129, 12, v127
	v_add_u32_e32 v129, 10, v124
	v_mul_u32_u24_e32 v130, 11, v129
	v_lshrrev_b32_e32 v130, 5, v130
	v_mul_u32_u24_e32 v169, 0x3000, v130
	v_lshl_add_u32 v169, v129, 12, v169
	v_add_u32_e32 v169, v169, v126
	global_load_dwordx4 v[152:155], v169, s[0:1]
	v_lshl_add_u32 v177, v129, 12, v127
	v_add_u32_e32 v129, 12, v124
	v_mul_u32_u24_e32 v130, 11, v129
	v_lshrrev_b32_e32 v130, 5, v130
	v_mul_u32_u24_e32 v170, 0x3000, v130
	v_lshl_add_u32 v170, v129, 12, v170
	v_add_u32_e32 v170, v170, v126
	global_load_dwordx4 v[156:159], v170, s[0:1]
	v_lshl_add_u32 v178, v129, 12, v127
	v_add_u32_e32 v129, 14, v124
	v_mul_u32_u24_e32 v130, 11, v129
	v_lshrrev_b32_e32 v130, 5, v130
	v_mul_u32_u24_e32 v171, 0x3000, v130
	v_lshl_add_u32 v171, v129, 12, v171
	v_add_u32_e32 v171, v171, v126
	global_load_dwordx4 v[160:163], v171, s[0:1]
	v_lshl_add_u32 v179, v129, 12, v127
	s_waitcnt vmcnt(7)
	ds_write_b128 v172, v[132:135]
	s_waitcnt vmcnt(6)
	ds_write_b128 v173, v[136:139]
	s_waitcnt vmcnt(5)
	ds_write_b128 v174, v[140:143]
	s_waitcnt vmcnt(4)
	ds_write_b128 v175, v[144:147]
	s_waitcnt vmcnt(3)
	ds_write_b128 v176, v[148:151]
	s_waitcnt vmcnt(2)
	ds_write_b128 v177, v[152:155]
	s_waitcnt vmcnt(1)
	ds_write_b128 v178, v[156:159]
	s_waitcnt vmcnt(0)
	ds_write_b128 v179, v[160:163]

.LBB0_885:
	s_lshr_b32 s8, s66, 13
	s_mulk_i32 s8, 0x3000
	s_and_b64 s[0:1], s[0:1], exec
	s_cselect_b32 s0, 0xc000, s8
	s_lshl_b64 s[8:9], s[10:11], 10
	s_lshl_b64 s[10:11], s[10:11], 11
	v_lshl_add_u64 v[34:35], v[82:83], 0, s[10:11]
	global_load_dwordx4 v[98:101], v[34:35], off
	global_load_dwordx4 v[102:105], v[34:35], off offset:16
	v_add_u32_e32 v38, s0, v67
	ds_read_b128 v[70:73], v38 offset:32768
	ds_read_b128 v[106:109], v38 offset:33792
	ds_read_b128 v[110:113], v38 offset:34816
	ds_read_b128 v[92:95], v38 offset:35840
	ds_read_b128 v[62:65], v38 offset:40960
	ds_read_b128 v[114:117], v38 offset:41984
	ds_read_b128 v[118:121], v38 offset:43008
	ds_read_b128 v[34:37], v38 offset:44032
	ds_read_b128 v[50:53], v38 offset:36864
	ds_read_b128 v[46:49], v38 offset:37888
	ds_read_b128 v[42:45], v38 offset:38912
	ds_read_b128 v[38:41], v38 offset:39936
	s_waitcnt lgkmcnt(7)
	v_pk_add_f32 v[62:63], v[62:63], 1.0 op_sel_hi:[1,0]
	s_waitcnt lgkmcnt(4)
	v_pk_add_f32 v[34:35], v[34:35], 1.0 op_sel_hi:[1,0]
	s_add_u32 s2, s2, s4
	s_addc_u32 s3, s3, s5
	v_lshl_add_u64 v[90:91], v[90:91], 0, s[6:7]
	s_cmp_lt_i32 s2, 0x8400
	s_waitcnt vmcnt(0)
	v_lshlrev_b32_e32 v122, 16, v105
	v_and_b32_e32 v123, 0xffff0000, v105
	v_pk_mul_f32 v[94:95], v[94:95], v[122:123]
	v_and_b32_e32 v105, 0xffff0000, v100
	v_pk_fma_f32 v[80:81], v[80:81], s[82:83], v[94:95] op_sel_hi:[1,0,1]
	v_lshlrev_b32_e32 v94, 16, v104
	v_and_b32_e32 v95, 0xffff0000, v104
	v_pk_mul_f32 v[92:93], v[92:93], v[94:95]
	v_lshlrev_b32_e32 v104, 16, v100
	v_pk_fma_f32 v[78:79], v[78:79], s[82:83], v[92:93] op_sel_hi:[1,0,1]
	v_lshlrev_b32_e32 v92, 16, v103
	v_and_b32_e32 v93, 0xffff0000, v103
	v_lshlrev_b32_e32 v94, 16, v102
	v_and_b32_e32 v95, 0xffff0000, v102
	v_lshlrev_b32_e32 v102, 16, v101
	v_and_b32_e32 v103, 0xffff0000, v101
	v_pk_mul_f32 v[100:101], v[106:107], v[104:105]
	v_lshlrev_b32_e32 v104, 16, v99
	v_and_b32_e32 v105, 0xffff0000, v99
	v_pk_mul_f32 v[72:73], v[72:73], v[104:105]
	v_pk_fma_f32 v[100:101], v[58:59], s[82:83], v[100:101] op_sel_hi:[1,0,1]
	v_pk_fma_f32 v[72:73], v[56:57], s[82:83], v[72:73] op_sel_hi:[1,0,1]
	v_pk_add_f32 v[56:57], v[64:65], 1.0 op_sel_hi:[1,0]
	v_lshlrev_b32_e32 v64, 16, v98
	v_and_b32_e32 v65, 0xffff0000, v98
	v_pk_mul_f32 v[64:65], v[70:71], v[64:65]
	v_pk_mul_f32 v[102:103], v[108:109], v[102:103]
	v_pk_fma_f32 v[54:55], v[54:55], s[82:83], v[64:65] op_sel_hi:[1,0,1]
	v_pk_fma_f32 v[102:103], v[60:61], s[82:83], v[102:103] op_sel_hi:[1,0,1]
	v_add_f32_e32 v64, 0, v54
	v_add_f32_e32 v64, v55, v64
	v_add_f32_e32 v64, v72, v64
	v_add_f32_e32 v64, v73, v64
	v_add_f32_e32 v64, v100, v64
	v_add_f32_e32 v64, v101, v64
	v_pk_mul_f32 v[94:95], v[110:111], v[94:95]
	v_add_f32_e32 v64, v102, v64
	v_pk_fma_f32 v[94:95], v[74:75], s[82:83], v[94:95] op_sel_hi:[1,0,1]
	v_add_f32_e32 v64, v103, v64
	v_pk_mul_f32 v[92:93], v[112:113], v[92:93]
	v_add_f32_e32 v64, v94, v64
	v_pk_fma_f32 v[92:93], v[76:77], s[82:83], v[92:93] op_sel_hi:[1,0,1]
	v_add_f32_e32 v64, v95, v64
	v_add_f32_e32 v64, v92, v64
	v_add_f32_e32 v64, v93, v64
	v_add_f32_e32 v64, v78, v64
	v_add_f32_e32 v64, v79, v64
	v_add_f32_e32 v64, v80, v64
	v_add_f32_e32 v64, v81, v64
	v_pk_add_f32 v[58:59], v[114:115], 1.0 op_sel_hi:[1,0]
	v_pk_add_f32 v[60:61], v[116:117], 1.0 op_sel_hi:[1,0]
	v_add_f32_dpp v64, v64, v64 quad_perm:[1,0,3,2] row_mask:0xf bank_mask:0xf bound_ctrl:1
	v_pk_add_f32 v[74:75], v[118:119], 1.0 op_sel_hi:[1,0]
	v_pk_add_f32 v[76:77], v[120:121], 1.0 op_sel_hi:[1,0]
	v_add_f32_dpp v64, v64, v64 quad_perm:[2,3,0,1] row_mask:0xf bank_mask:0xf bound_ctrl:1
	s_nop 1
	v_add_f32_dpp v64, v64, v64 row_half_mirror row_mask:0xf bank_mask:0xf bound_ctrl:1
	s_nop 1
	v_add_f32_dpp v64, v64, v64 row_mirror row_mask:0xf bank_mask:0xf bound_ctrl:1
	s_nop 0
	v_readlane_b32 s12, v64, 16
	v_readlane_b32 s13, v64, 48
	v_readlane_b32 s0, v64, 0
	v_readlane_b32 s1, v64, 32
	v_mov_b32_e32 v64, s12
	v_mov_b32_e32 v65, s13
	v_pk_add_f32 v[64:65], s[0:1], v[64:65]
	s_nop 0
	v_add_f32_e32 v64, v64, v65
	v_mul_f32_e32 v64, 0x3a800000, v64
	v_pk_add_f32 v[54:55], v[54:55], v[64:65] op_sel_hi:[1,0] neg_lo:[0,1] neg_hi:[0,1]
	v_pk_add_f32 v[72:73], v[72:73], v[64:65] op_sel_hi:[1,0] neg_lo:[0,1] neg_hi:[0,1]
	v_pk_mul_f32 v[70:71], v[54:55], v[54:55]
	v_pk_mul_f32 v[98:99], v[72:73], v[72:73]
	v_add_f32_e32 v70, v70, v71
	v_pk_add_f32 v[100:101], v[100:101], v[64:65] op_sel_hi:[1,0] neg_lo:[0,1] neg_hi:[0,1]
	v_add_f32_e32 v70, v98, v70
	v_pk_mul_f32 v[104:105], v[100:101], v[100:101]
	v_add_f32_e32 v70, v99, v70
	v_pk_add_f32 v[102:103], v[102:103], v[64:65] op_sel_hi:[1,0] neg_lo:[0,1] neg_hi:[0,1]
	v_add_f32_e32 v70, v104, v70
	v_pk_mul_f32 v[106:107], v[102:103], v[102:103]
	v_add_f32_e32 v70, v105, v70
	v_pk_add_f32 v[94:95], v[94:95], v[64:65] op_sel_hi:[1,0] neg_lo:[0,1] neg_hi:[0,1]
	v_add_f32_e32 v70, v106, v70
	v_pk_mul_f32 v[108:109], v[94:95], v[94:95]
	v_add_f32_e32 v70, v107, v70
	v_pk_add_f32 v[92:93], v[92:93], v[64:65] op_sel_hi:[1,0] neg_lo:[0,1] neg_hi:[0,1]
	v_add_f32_e32 v70, v108, v70
	v_pk_mul_f32 v[110:111], v[92:93], v[92:93]
	v_add_f32_e32 v70, v109, v70
	v_pk_add_f32 v[78:79], v[78:79], v[64:65] op_sel_hi:[1,0] neg_lo:[0,1] neg_hi:[0,1]
	v_add_f32_e32 v70, v110, v70
	v_pk_mul_f32 v[112:113], v[78:79], v[78:79]
	v_add_f32_e32 v70, v111, v70
	v_pk_add_f32 v[64:65], v[80:81], v[64:65] op_sel_hi:[1,0] neg_lo:[0,1] neg_hi:[0,1]
	v_add_f32_e32 v70, v112, v70
	v_pk_mul_f32 v[80:81], v[64:65], v[64:65]
	v_add_f32_e32 v70, v113, v70
	v_add_f32_e32 v70, v80, v70
	v_add_f32_e32 v70, v81, v70
	s_nop 1
	v_add_f32_dpp v70, v70, v70 quad_perm:[1,0,3,2] row_mask:0xf bank_mask:0xf bound_ctrl:1
	s_nop 1
	v_add_f32_dpp v70, v70, v70 quad_perm:[2,3,0,1] row_mask:0xf bank_mask:0xf bound_ctrl:1
	s_nop 1
	v_add_f32_dpp v70, v70, v70 row_half_mirror row_mask:0xf bank_mask:0xf bound_ctrl:1
	s_nop 1
	v_add_f32_dpp v70, v70, v70 row_mirror row_mask:0xf bank_mask:0xf bound_ctrl:1
	s_nop 0
	v_readlane_b32 s12, v70, 16
	v_readlane_b32 s13, v70, 48
	v_readlane_b32 s0, v70, 0
	v_readlane_b32 s1, v70, 32
	v_mov_b32_e32 v70, s12
	v_mov_b32_e32 v71, s13
	v_pk_add_f32 v[70:71], s[0:1], v[70:71]
	s_nop 0
	v_add_f32_e32 v70, v70, v71
	v_fmamk_f32 v70, v70, 0x3a800000, v236
	v_cmp_gt_f32_e32 vcc, s93, v70
	v_mul_f32_e32 v71, 0x4b800000, v70
	s_nop 0
	v_cndmask_b32_e32 v70, v70, v71, vcc
	v_rsq_f32_e32 v70, v70
	s_nop 0
	v_mul_f32_e32 v71, 0x45800000, v70
	v_cndmask_b32_e32 v70, v70, v71, vcc
	v_pk_mul_f32 v[54:55], v[54:55], v[70:71] op_sel_hi:[1,0]
	s_nop 0
	v_pk_fma_f32 v[54:55], v[14:15], v[54:55], v[30:31]
	s_waitcnt lgkmcnt(3)
	v_pk_fma_f32 v[50:51], v[62:63], v[54:55], v[50:51]
	v_pk_mul_f32 v[62:63], v[72:73], v[70:71] op_sel_hi:[1,0]
	v_pk_mul_f32 v[72:73], v[92:93], v[70:71] op_sel_hi:[1,0]
	v_pk_fma_f32 v[62:63], v[16:17], v[62:63], v[32:33]
	v_pk_fma_f32 v[72:73], v[8:9], v[72:73], v[24:25]
	v_pk_fma_f32 v[52:53], v[56:57], v[62:63], v[52:53]
	v_pk_mul_f32 v[56:57], v[100:101], v[70:71] op_sel_hi:[1,0]
	s_waitcnt lgkmcnt(1)
	v_pk_fma_f32 v[44:45], v[76:77], v[72:73], v[44:45]
	v_pk_fma_f32 v[56:57], v[10:11], v[56:57], v[26:27]
	s_nop 0
	v_pk_fma_f32 v[46:47], v[58:59], v[56:57], v[46:47]
	v_pk_mul_f32 v[58:59], v[102:103], v[70:71] op_sel_hi:[1,0]
	s_nop 0
	v_pk_fma_f32 v[58:59], v[12:13], v[58:59], v[28:29]
	s_nop 0
	v_pk_fma_f32 v[48:49], v[60:61], v[58:59], v[48:49]
	v_pk_mul_f32 v[60:61], v[94:95], v[70:71] op_sel_hi:[1,0]
	s_nop 0
	v_pk_fma_f32 v[60:61], v[6:7], v[60:61], v[22:23]
	s_nop 0
	v_pk_fma_f32 v[42:43], v[74:75], v[60:61], v[42:43]
	v_pk_mul_f32 v[74:75], v[78:79], v[70:71] op_sel_hi:[1,0]
	s_nop 0
	v_pk_fma_f32 v[74:75], v[2:3], v[74:75], v[18:19]
	s_waitcnt lgkmcnt(0)
	v_pk_fma_f32 v[76:77], v[34:35], v[74:75], v[38:39]
	v_pk_mul_f32 v[34:35], v[64:65], v[70:71] op_sel_hi:[1,0]
	s_nop 0
	v_pk_fma_f32 v[38:39], v[4:5], v[34:35], v[20:21]
	v_pk_add_f32 v[34:35], v[36:37], 1.0 op_sel_hi:[1,0]
	v_cvt_pk_bf16_f32 v36, v56, v57
	v_pk_fma_f32 v[64:65], v[34:35], v[38:39], v[40:41]
	v_cvt_pk_bf16_f32 v34, v54, v55
	v_cvt_pk_bf16_f32 v35, v62, v63
	v_cvt_pk_bf16_f32 v37, v58, v59
	ds_write_b128 v96, v[34:37]
	v_cvt_pk_bf16_f32 v34, v60, v61
	v_cvt_pk_bf16_f32 v35, v72, v73
	v_cvt_pk_bf16_f32 v36, v74, v75
	v_cvt_pk_bf16_f32 v37, v38, v39
	ds_write_b128 v96, v[34:37] offset:16
	ds_read_b128 v[34:37], v97
	ds_read_b128 v[38:41], v97 offset:1024
	v_lshl_add_u64 v[54:55], v[86:87], 0, s[10:11]
	s_waitcnt lgkmcnt(1)
	global_store_dwordx4 v[54:55], v[34:37], off sc1
	s_waitcnt lgkmcnt(0)
	global_store_dwordx4 v[54:55], v[38:41], off offset:1024 sc1
	v_cvt_pk_bf16_f32 v34, v50, v51
	v_cvt_pk_bf16_f32 v35, v52, v53
	v_cvt_pk_bf16_f32 v36, v46, v47
	v_cvt_pk_bf16_f32 v37, v48, v49
	ds_write_b128 v96, v[34:37]
	v_cvt_pk_bf16_f32 v34, v42, v43
	v_cvt_pk_bf16_f32 v35, v44, v45
	v_cvt_pk_bf16_f32 v36, v76, v77
	v_cvt_pk_bf16_f32 v37, v64, v65
	ds_write_b128 v96, v[34:37] offset:16
	ds_read_b128 v[34:37], v97
	ds_read_b128 v[38:41], v97 offset:1024
	v_lshl_add_u64 v[54:55], v[88:89], 0, s[10:11]
	s_waitcnt lgkmcnt(1)
	global_store_dwordx4 v[54:55], v[34:37], off sc1
	s_waitcnt lgkmcnt(0)
	global_store_dwordx4 v[54:55], v[38:41], off offset:1024 sc1
	v_mov_b32_e32 v34, v69
	v_mov_b32_e32 v35, v69
	v_mov_b32_e32 v36, v69
	v_mov_b32_e32 v37, v69
	v_cvt_pk_fp8_f32 v34, v50, v51
	v_cvt_pk_fp8_f32 v35, v46, v47
	v_cvt_pk_fp8_f32 v36, v42, v43
	v_cvt_pk_fp8_f32 v37, v76, v77
	v_cvt_pk_fp8_f32 v34, v52, v53 op_sel:[0,0,1]
	v_cvt_pk_fp8_f32 v35, v48, v49 op_sel:[0,0,1]
	v_cvt_pk_fp8_f32 v36, v44, v45 op_sel:[0,0,1]
	v_cvt_pk_fp8_f32 v37, v64, v65 op_sel:[0,0,1]
	v_lshl_add_u64 v[38:39], v[84:85], 0, s[8:9]
	global_store_dwordx4 v[38:39], v[34:37], off sc1
	s_cbranch_scc0 .LBB0_893
